# P4 fixup/gMLP: prefetch no longer drained by early vmcnt(0) (gn preloaded once, loop-carried copies at the end); P10 epilogue loads de-serialized; P7 tail edits
# baseline (speedup 1.0000x reference)
_Z6mk_fwd4Args:
	s_mov_b32 s100, -1
	s_mov_b32 s98, 0
	s_load_dword s84, s[0:1], 0xd0
	s_load_dwordx4 s[4:7], s[0:1], 0xc0
	s_mov_b32 s87, s2
	s_add_u32 s2, s0, 0xd0
	s_addc_u32 s3, s1, 0
	v_readfirstlane_b32 s92, v0
	s_waitcnt lgkmcnt(0)
	v_writelane_b32 v242, s4, 0
	s_mov_b32 s93, s87
	s_nop 0
	v_writelane_b32 v242, s5, 1
	v_writelane_b32 v242, s6, 2
	v_writelane_b32 v242, s7, 3
	v_writelane_b32 v242, s2, 4
	s_nop 1
	v_writelane_b32 v242, s3, 5
	s_and_b32 s3, s84, 7
	s_mov_b32 s2, 0
	s_cmp_lg_u32 s3, 0
	s_cbranch_scc1 .LBB0_2
	s_ashr_i32 s4, s87, 31
	s_lshr_b32 s4, s4, 29
	s_add_i32 s4, s87, s4
	s_and_b32 s5, s4, -8
	s_ashr_i32 s3, s84, 3
	s_sub_i32 s5, s87, s5
	s_mul_i32 s3, s3, s5
	s_ashr_i32 s4, s4, 3
	s_add_i32 s93, s3, s4

.LBB0_398:
	v_mov_b32_e32 v150, v79
	v_mov_b32_e32 v151, v75
	v_mov_b32_e32 v138, v78
	v_mov_b32_e32 v139, v74
	v_pk_mul_f32 v[150:151], v[150:151], v[150:151]
	v_mov_b32_e32 v152, v81
	v_mov_b32_e32 v153, v77
	v_pk_fma_f32 v[138:139], v[138:139], v[138:139], v[150:151]
	v_mov_b32_e32 v150, v80
	v_mov_b32_e32 v151, v76
	v_pk_mul_f32 v[152:153], v[152:153], v[152:153]
	s_and_b32 s6, s20, 0xe0
	v_pk_fma_f32 v[150:151], v[150:151], v[150:151], v[152:153]
	v_pk_mul_f32 v[152:153], v[70:71], v[70:71]
	v_pk_add_f32 v[138:139], v[138:139], v[150:151]
	v_pk_mul_f32 v[150:151], v[72:73], v[72:73]
	v_or_b32_e32 v160, s6, v142
	v_pk_mov_b32 v[154:155], v[152:153], v[150:151] op_sel:[1,0]
	v_mov_b32_e32 v153, v151
	v_lshlrev_b32_e32 v161, 4, v160
	v_pk_add_f32 v[154:155], v[154:155], v[152:153]
	s_cmp_eq_u32 s6, s100
	s_cbranch_scc1 .Lfx_gn_ready
	global_load_dwordx4 v[196:199], v161, s[46:47]
	global_load_dwordx4 v[200:203], v161, s[46:47] offset:64
	global_load_dwordx4 v[204:207], v161, s[46:47] offset:128
	global_load_dwordx4 v[208:211], v161, s[46:47] offset:192
	global_load_dwordx4 v[212:215], v161, s[46:47] offset:256
	global_load_dwordx4 v[216:219], v161, s[46:47] offset:320
	global_load_dwordx4 v[224:227], v161, s[46:47] offset:384
	global_load_dwordx4 v[228:231], v161, s[46:47] offset:448
	s_mov_b32 s100, s6
	s_waitcnt vmcnt(0)
.Lfx_gn_ready:
	v_mov_b64_e32 v[150:151], v[196:197]
	v_mov_b64_e32 v[152:153], v[198:199]
	v_mul_f32_e32 v93, v62, v62
	v_mul_f32_e32 v94, v63, v63
	v_pk_add_f32 v[138:139], v[138:139], v[138:139] op_sel:[0,1] op_sel_hi:[1,0]
	v_pk_add_f32 v[154:155], v[154:155], v[154:155] op_sel:[0,1] op_sel_hi:[1,0]
	v_mov_b32_e32 v139, v93
	v_mov_b32_e32 v155, v94
	v_mul_f32_e32 v94, v67, v67
	v_pk_add_f32 v[138:139], v[138:139], v[154:155]
	v_pk_fma_f32 v[154:155], v[66:67], v[66:67], v[94:95] op_sel_hi:[1,1,0]
	v_mul_f32_e32 v94, v69, v69
	v_mul_f32_e32 v140, v64, v64
	v_mul_f32_e32 v158, v65, v65
	v_pk_fma_f32 v[156:157], v[68:69], v[68:69], v[94:95] op_sel_hi:[1,1,0]
	v_mov_b32_e32 v155, v140
	v_mov_b32_e32 v157, v158
	v_pk_add_f32 v[154:155], v[154:155], v[156:157]
	v_pk_mul_f32 v[156:157], v[58:59], v[58:59]
	v_pk_add_f32 v[138:139], v[138:139], v[154:155]
	v_pk_mul_f32 v[154:155], v[60:61], v[60:61]
	v_mul_f32_e32 v93, v50, v50
	v_pk_mov_b32 v[158:159], v[156:157], v[154:155] op_sel:[1,0]
	v_mov_b32_e32 v157, v155
	v_pk_add_f32 v[154:155], v[158:159], v[156:157]
	v_mul_f32_e32 v94, v51, v51
	v_pk_add_f32 v[138:139], v[138:139], v[138:139] op_sel:[0,1] op_sel_hi:[1,0]
	v_pk_add_f32 v[154:155], v[154:155], v[154:155] op_sel:[0,1] op_sel_hi:[1,0]
	v_mov_b32_e32 v139, v93
	v_mov_b32_e32 v155, v94
	v_mul_f32_e32 v94, v55, v55
	v_pk_add_f32 v[138:139], v[138:139], v[154:155]
	v_pk_fma_f32 v[154:155], v[54:55], v[54:55], v[94:95] op_sel_hi:[1,1,0]
	v_mul_f32_e32 v94, v57, v57
	v_mul_f32_e32 v140, v52, v52
	v_mul_f32_e32 v158, v53, v53
	v_pk_fma_f32 v[156:157], v[56:57], v[56:57], v[94:95] op_sel_hi:[1,1,0]
	v_mov_b32_e32 v155, v140
	v_mov_b32_e32 v157, v158
	v_pk_add_f32 v[154:155], v[154:155], v[156:157]
	s_lshl_b32 s6, s21, 7
	v_pk_add_f32 v[138:139], v[138:139], v[154:155]
	s_and_b32 s12, s14, 0xfffff000
	v_add_f32_e32 v93, v138, v139
	ds_bpermute_b32 v94, v144, v93
	s_or_b32 s6, s12, s6
	v_add_u32_e32 v138, s6, v143
	v_ashrrev_i32_e32 v139, 31, v138
	v_lshlrev_b64 v[138:139], 12, v[138:139]
	s_waitcnt lgkmcnt(0)
	v_add_f32_e32 v93, v93, v94
	ds_bpermute_b32 v94, v145, v93
	v_lshl_add_u64 v[138:139], s[74:75], 0, v[138:139]
	s_add_i32 s14, s14, s15
	s_mov_b32 s20, s19
	s_waitcnt lgkmcnt(0)
	v_add_f32_e32 v93, v93, v94
	v_fmamk_f32 v93, v93, 0x3c000000, v149
	v_mul_f32_e32 v94, 0x4b800000, v93
	v_cmp_gt_f32_e32 vcc, s18, v93
	s_nop 1
	v_cndmask_b32_e32 v93, v93, v94, vcc
	v_rsq_f32_e32 v93, v93
	s_nop 0
	v_mul_f32_e32 v94, 0x45800000, v93
	v_cndmask_b32_e32 v140, v93, v94, vcc
	v_lshlrev_b32_e32 v93, 16, v136
	v_mul_f32_e32 v93, 0xbfb8aa3b, v93
	v_and_b32_e32 v94, 0xffff0000, v136
	v_exp_f32_e32 v93, v93
	v_mul_f32_e32 v94, 0xbfb8aa3b, v94
	v_exp_f32_e32 v94, v94
	v_pk_mul_f32 v[78:79], v[140:141], v[78:79] op_sel_hi:[0,1]
	v_add_f32_e32 v93, 1.0, v93
	v_rcp_f32_e32 v154, v93
	v_add_f32_e32 v93, 1.0, v94
	v_rcp_f32_e32 v155, v93
	v_lshlrev_b32_e32 v93, 16, v137
	v_mul_f32_e32 v93, 0xbfb8aa3b, v93
	v_and_b32_e32 v94, 0xffff0000, v137
	v_exp_f32_e32 v93, v93
	v_mul_f32_e32 v94, 0xbfb8aa3b, v94
	v_exp_f32_e32 v94, v94
	v_pk_mul_f32 v[80:81], v[140:141], v[80:81] op_sel_hi:[0,1]
	v_add_f32_e32 v93, 1.0, v93
	v_rcp_f32_e32 v136, v93
	v_add_f32_e32 v93, 1.0, v94
	v_rcp_f32_e32 v137, v93
	v_pk_mul_f32 v[78:79], v[150:151], v[78:79]
	v_pk_mul_f32 v[80:81], v[152:153], v[80:81]
	v_pk_mul_f32 v[78:79], v[78:79], v[154:155]
	v_pk_mul_f32 v[80:81], v[80:81], v[136:137]
	v_lshlrev_b32_e32 v94, 3, v160
	v_cvt_pk_bf16_f32 v136, v78, v79
	v_cvt_pk_bf16_f32 v137, v80, v81
	v_lshl_add_u64 v[78:79], v[138:139], 0, v[94:95]
	global_store_dwordx2 v[78:79], v[136:137], off
	s_nop 1
	v_mov_b64_e32 v[136:137], v[200:201]
	v_mov_b64_e32 v[138:139], v[202:203]
	v_lshlrev_b32_e32 v80, 16, v102
	v_and_b32_e32 v81, 0xffff0000, v102
	v_lshlrev_b32_e32 v93, 16, v103
	v_and_b32_e32 v94, 0xffff0000, v103
	v_mul_f32_e32 v80, 0xbfb8aa3b, v80
	v_mul_f32_e32 v81, 0xbfb8aa3b, v81
	v_mul_f32_e32 v93, 0xbfb8aa3b, v93
	v_mul_f32_e32 v94, 0xbfb8aa3b, v94
	v_exp_f32_e32 v80, v80
	v_exp_f32_e32 v81, v81
	v_exp_f32_e32 v93, v93
	v_exp_f32_e32 v94, v94
	v_add_f32_e32 v80, 1.0, v80
	v_add_f32_e32 v81, 1.0, v81
	v_add_f32_e32 v93, 1.0, v93
	v_add_f32_e32 v94, 1.0, v94
	v_rcp_f32_e32 v80, v80
	v_rcp_f32_e32 v81, v81
	v_rcp_f32_e32 v102, v93
	v_rcp_f32_e32 v103, v94
	v_pk_mul_f32 v[74:75], v[140:141], v[74:75] op_sel_hi:[0,1]
	v_pk_mul_f32 v[76:77], v[140:141], v[76:77] op_sel_hi:[0,1]
	v_lshlrev_b32_e32 v93, 16, v101
	v_and_b32_e32 v94, 0xffff0000, v101
	v_mul_f32_e32 v93, 0xbfb8aa3b, v93
	v_mul_f32_e32 v94, 0xbfb8aa3b, v94
	v_exp_f32_e32 v93, v93
	v_exp_f32_e32 v94, v94
	v_pk_mul_f32 v[70:71], v[140:141], v[70:71] op_sel_hi:[0,1]
	v_pk_mul_f32 v[72:73], v[140:141], v[72:73] op_sel_hi:[0,1]
	v_add_f32_e32 v93, 1.0, v93
	v_add_f32_e32 v94, 1.0, v94
	v_rcp_f32_e32 v101, v94
	v_pk_mul_f32 v[66:67], v[140:141], v[66:67] op_sel_hi:[0,1]
	v_pk_mul_f32 v[68:69], v[140:141], v[68:69] op_sel_hi:[0,1]
	v_pk_mul_f32 v[62:63], v[140:141], v[62:63] op_sel_hi:[0,1]
	v_pk_mul_f32 v[64:65], v[140:141], v[64:65] op_sel_hi:[0,1]
	v_pk_mul_f32 v[58:59], v[140:141], v[58:59] op_sel_hi:[0,1]
	v_pk_mul_f32 v[60:61], v[140:141], v[60:61] op_sel_hi:[0,1]
	v_pk_mul_f32 v[54:55], v[140:141], v[54:55] op_sel_hi:[0,1]
	v_pk_mul_f32 v[56:57], v[140:141], v[56:57] op_sel_hi:[0,1]
	v_pk_mul_f32 v[50:51], v[140:141], v[50:51] op_sel_hi:[0,1]
	v_pk_mul_f32 v[52:53], v[140:141], v[52:53] op_sel_hi:[0,1]
	s_and_b64 vcc, exec, s[10:11]
	v_pk_mul_f32 v[74:75], v[136:137], v[74:75]
	v_pk_mul_f32 v[76:77], v[138:139], v[76:77]
	v_pk_mul_f32 v[74:75], v[74:75], v[80:81]
	v_pk_mul_f32 v[76:77], v[76:77], v[102:103]
	v_cvt_pk_bf16_f32 v74, v74, v75
	v_cvt_pk_bf16_f32 v75, v76, v77
	global_store_dwordx2 v[78:79], v[74:75], off offset:32
	s_nop 1
	v_mov_b64_e32 v[74:75], v[204:205]
	v_mov_b64_e32 v[76:77], v[206:207]
	v_lshlrev_b32_e32 v80, 16, v100
	v_and_b32_e32 v81, 0xffff0000, v100
	v_mul_f32_e32 v80, 0xbfb8aa3b, v80
	v_mul_f32_e32 v81, 0xbfb8aa3b, v81
	v_exp_f32_e32 v80, v80
	v_exp_f32_e32 v81, v81
	v_rcp_f32_e32 v100, v93
	v_add_f32_e32 v80, 1.0, v80
	v_add_f32_e32 v81, 1.0, v81
	v_rcp_f32_e32 v80, v80
	v_rcp_f32_e32 v81, v81
	v_pk_mul_f32 v[70:71], v[74:75], v[70:71]
	v_pk_mul_f32 v[72:73], v[76:77], v[72:73]
	v_pk_mul_f32 v[70:71], v[70:71], v[80:81]
	v_pk_mul_f32 v[72:73], v[72:73], v[100:101]
	v_cvt_pk_bf16_f32 v70, v70, v71
	v_cvt_pk_bf16_f32 v71, v72, v73
	global_store_dwordx2 v[78:79], v[70:71], off offset:64
	s_nop 1
	v_mov_b64_e32 v[70:71], v[208:209]
	v_mov_b64_e32 v[72:73], v[210:211]
	v_lshlrev_b32_e32 v74, 16, v98
	v_and_b32_e32 v75, 0xffff0000, v98
	v_lshlrev_b32_e32 v76, 16, v99
	v_and_b32_e32 v77, 0xffff0000, v99
	v_mul_f32_e32 v74, 0xbfb8aa3b, v74
	v_mul_f32_e32 v75, 0xbfb8aa3b, v75
	v_mul_f32_e32 v76, 0xbfb8aa3b, v76
	v_mul_f32_e32 v77, 0xbfb8aa3b, v77
	v_exp_f32_e32 v74, v74
	v_exp_f32_e32 v75, v75
	v_exp_f32_e32 v76, v76
	v_exp_f32_e32 v77, v77
	v_add_f32_e32 v74, 1.0, v74
	v_add_f32_e32 v75, 1.0, v75
	v_add_f32_e32 v76, 1.0, v76
	v_add_f32_e32 v77, 1.0, v77
	v_rcp_f32_e32 v74, v74
	v_rcp_f32_e32 v75, v75
	v_rcp_f32_e32 v76, v76
	v_rcp_f32_e32 v77, v77
	v_pk_mul_f32 v[66:67], v[70:71], v[66:67]
	v_pk_mul_f32 v[68:69], v[72:73], v[68:69]
	v_pk_mul_f32 v[66:67], v[66:67], v[74:75]
	v_pk_mul_f32 v[68:69], v[68:69], v[76:77]
	v_cvt_pk_bf16_f32 v66, v66, v67
	v_cvt_pk_bf16_f32 v67, v68, v69
	global_store_dwordx2 v[78:79], v[66:67], off offset:96
	s_nop 1
	v_mov_b64_e32 v[66:67], v[212:213]
	v_mov_b64_e32 v[68:69], v[214:215]
	v_lshlrev_b32_e32 v70, 16, v96
	v_and_b32_e32 v71, 0xffff0000, v96
	v_lshlrev_b32_e32 v72, 16, v97
	v_and_b32_e32 v73, 0xffff0000, v97
	v_mul_f32_e32 v70, 0xbfb8aa3b, v70
	v_mul_f32_e32 v71, 0xbfb8aa3b, v71
	v_mul_f32_e32 v72, 0xbfb8aa3b, v72
	v_mul_f32_e32 v73, 0xbfb8aa3b, v73
	v_exp_f32_e32 v70, v70
	v_exp_f32_e32 v71, v71
	v_exp_f32_e32 v72, v72
	v_exp_f32_e32 v73, v73
	v_add_f32_e32 v70, 1.0, v70
	v_add_f32_e32 v71, 1.0, v71
	v_add_f32_e32 v72, 1.0, v72
	v_add_f32_e32 v73, 1.0, v73
	v_rcp_f32_e32 v70, v70
	v_rcp_f32_e32 v71, v71
	v_rcp_f32_e32 v72, v72
	v_rcp_f32_e32 v73, v73
	v_lshlrev_b32_e32 v74, 16, v85
	v_and_b32_e32 v75, 0xffff0000, v85
	v_mul_f32_e32 v74, 0xbfb8aa3b, v74
	v_mul_f32_e32 v75, 0xbfb8aa3b, v75
	v_exp_f32_e32 v74, v74
	v_exp_f32_e32 v75, v75
	v_add_f32_e32 v74, 1.0, v74
	v_add_f32_e32 v75, 1.0, v75
	v_rcp_f32_e32 v74, v74
	v_rcp_f32_e32 v75, v75
	v_pk_mul_f32 v[62:63], v[66:67], v[62:63]
	v_pk_mul_f32 v[64:65], v[68:69], v[64:65]
	v_pk_mul_f32 v[62:63], v[62:63], v[70:71]
	v_pk_mul_f32 v[64:65], v[64:65], v[72:73]
	v_cvt_pk_bf16_f32 v62, v62, v63
	v_cvt_pk_bf16_f32 v63, v64, v65
	global_store_dwordx2 v[78:79], v[62:63], off offset:128
	s_nop 1
	v_mov_b64_e32 v[62:63], v[216:217]
	v_mov_b64_e32 v[64:65], v[218:219]
	v_lshlrev_b32_e32 v66, 16, v88
	v_and_b32_e32 v67, 0xffff0000, v88
	v_lshlrev_b32_e32 v68, 16, v89
	v_and_b32_e32 v69, 0xffff0000, v89
	v_mul_f32_e32 v66, 0xbfb8aa3b, v66
	v_mul_f32_e32 v67, 0xbfb8aa3b, v67
	v_mul_f32_e32 v68, 0xbfb8aa3b, v68
	v_mul_f32_e32 v69, 0xbfb8aa3b, v69
	v_exp_f32_e32 v66, v66
	v_exp_f32_e32 v67, v67
	v_exp_f32_e32 v68, v68
	v_exp_f32_e32 v69, v69
	v_add_f32_e32 v66, 1.0, v66
	v_add_f32_e32 v67, 1.0, v67
	v_add_f32_e32 v68, 1.0, v68
	v_add_f32_e32 v69, 1.0, v69
	v_rcp_f32_e32 v66, v66
	v_rcp_f32_e32 v67, v67
	v_rcp_f32_e32 v68, v68
	v_rcp_f32_e32 v69, v69
	v_lshlrev_b32_e32 v72, 16, v84
	v_and_b32_e32 v73, 0xffff0000, v84
	v_mul_f32_e32 v72, 0xbfb8aa3b, v72
	v_mul_f32_e32 v73, 0xbfb8aa3b, v73
	v_exp_f32_e32 v72, v72
	v_exp_f32_e32 v73, v73
	v_add_f32_e32 v72, 1.0, v72
	v_add_f32_e32 v73, 1.0, v73
	v_rcp_f32_e32 v72, v72
	v_rcp_f32_e32 v73, v73
	v_pk_mul_f32 v[58:59], v[62:63], v[58:59]
	v_pk_mul_f32 v[60:61], v[64:65], v[60:61]
	v_pk_mul_f32 v[58:59], v[58:59], v[66:67]
	v_pk_mul_f32 v[60:61], v[60:61], v[68:69]
	v_cvt_pk_bf16_f32 v58, v58, v59
	v_cvt_pk_bf16_f32 v59, v60, v61
	global_store_dwordx2 v[78:79], v[58:59], off offset:160
	s_nop 1
	v_mov_b64_e32 v[58:59], v[224:225]
	v_mov_b64_e32 v[60:61], v[226:227]
	v_lshlrev_b32_e32 v62, 16, v86
	v_and_b32_e32 v63, 0xffff0000, v86
	v_lshlrev_b32_e32 v64, 16, v87
	v_and_b32_e32 v65, 0xffff0000, v87
	v_mul_f32_e32 v62, 0xbfb8aa3b, v62
	v_mul_f32_e32 v63, 0xbfb8aa3b, v63
	v_mul_f32_e32 v64, 0xbfb8aa3b, v64
	v_mul_f32_e32 v65, 0xbfb8aa3b, v65
	v_exp_f32_e32 v62, v62
	v_exp_f32_e32 v63, v63
	v_exp_f32_e32 v64, v64
	v_exp_f32_e32 v65, v65
	v_add_f32_e32 v62, 1.0, v62
	v_add_f32_e32 v63, 1.0, v63
	v_add_f32_e32 v64, 1.0, v64
	v_add_f32_e32 v65, 1.0, v65
	v_rcp_f32_e32 v62, v62
	v_rcp_f32_e32 v63, v63
	v_rcp_f32_e32 v64, v64
	v_rcp_f32_e32 v65, v65
	v_pk_mul_f32 v[54:55], v[58:59], v[54:55]
	v_pk_mul_f32 v[56:57], v[60:61], v[56:57]
	v_pk_mul_f32 v[54:55], v[54:55], v[62:63]
	v_pk_mul_f32 v[56:57], v[56:57], v[64:65]
	v_cvt_pk_bf16_f32 v54, v54, v55
	v_cvt_pk_bf16_f32 v55, v56, v57
	global_store_dwordx2 v[78:79], v[54:55], off offset:192
	s_nop 1
	v_mov_b64_e32 v[68:69], v[228:229]
	v_mov_b64_e32 v[70:71], v[230:231]
	v_pk_mul_f32 v[50:51], v[68:69], v[50:51]
	v_pk_mul_f32 v[52:53], v[70:71], v[52:53]
	v_pk_mul_f32 v[50:51], v[50:51], v[72:73]
	v_pk_mul_f32 v[52:53], v[52:53], v[74:75]
	v_cvt_pk_bf16_f32 v50, v50, v51
	v_cvt_pk_bf16_f32 v51, v52, v53
	global_store_dwordx2 v[78:79], v[50:51], off offset:224
	s_waitcnt vmcnt(8)
	v_mov_b64_e32 v[136:137], v[128:129]
	v_mov_b64_e32 v[102:103], v[112:113]
	v_mov_b64_e32 v[138:139], v[126:127]
	v_mov_b64_e32 v[100:101], v[114:115]
	v_mov_b64_e32 v[98:99], v[116:117]
	v_mov_b64_e32 v[96:97], v[118:119]
	v_mov_b64_e32 v[88:89], v[130:131]
	v_mov_b64_e32 v[84:85], v[134:135]
	v_mov_b64_e32 v[86:87], v[132:133]
	v_mov_b64_e32 v[66:67], v[104:105]
	v_mov_b64_e32 v[64:65], v[106:107]
	v_mov_b64_e32 v[62:63], v[108:109]
	v_mov_b64_e32 v[60:61], v[110:111]
	v_mov_b64_e32 v[58:59], v[120:121]
	v_mov_b64_e32 v[54:55], v[122:123]
	v_mov_b64_e32 v[56:57], v[124:125]
	s_barrier
	s_cbranch_vccnz .LBB0_407

.LBB0_418:
	s_waitcnt vmcnt(0)
	s_add_i32 s4, s87, s84
	s_cmpk_gt_i32 s4, 0x3ff
	s_cselect_b64 s[68:69], -1, 0
	s_and_b64 vcc, exec, s[68:69]
	v_lshlrev_b32_e32 v146, 1, v148
	s_cbranch_vccnz .LBB0_422
	s_lshl_b32 s5, s4, 4
	s_and_b32 s5, s5, 0xffffff80
	v_add_u32_e32 v12, s5, v149
	v_mov_b64_e32 v[70:71], s[96:97]
	s_lshl_b32 s6, s4, 8
	v_mad_i64_i32 v[2:3], vcc, v12, s33, v[70:71]
	s_and_b32 s84, s6, 0x700
	v_lshl_add_u64 v[2:3], v[2:3], 0, s[84:85]
	v_lshlrev_b32_e32 v18, 1, v102
	v_lshl_add_u64 v[2:3], v[2:3], 0, v[18:19]
	v_add_co_u32_e32 v2, vcc, 0x2000, v2
	v_or_b32_e32 v4, 1, v12
	s_nop 0
	v_addc_co_u32_e32 v3, vcc, 0, v3, vcc
	v_mad_i64_i32 v[4:5], vcc, v4, s33, v[70:71]
	v_lshl_add_u64 v[4:5], v[4:5], 0, s[84:85]
	v_lshl_add_u64 v[4:5], v[4:5], 0, v[18:19]
	v_add_co_u32_e32 v6, vcc, 0x2000, v4
	v_or_b32_e32 v10, 2, v12
	s_nop 0
	v_addc_co_u32_e32 v7, vcc, 0, v5, vcc
	v_mad_i64_i32 v[10:11], vcc, v10, s33, v[70:71]
	v_lshl_add_u64 v[10:11], v[10:11], 0, s[84:85]
	v_lshl_add_u64 v[10:11], v[10:11], 0, v[18:19]
	v_add_co_u32_e32 v10, vcc, 0x2000, v10
	v_or_b32_e32 v12, 3, v12
	s_nop 0
	v_addc_co_u32_e32 v11, vcc, 0, v11, vcc
	v_mad_i64_i32 v[12:13], vcc, v12, s33, v[70:71]
	v_lshl_add_u64 v[12:13], v[12:13], 0, s[84:85]
	s_and_b32 s6, s4, 0xffffff8
	v_readlane_b32 s7, v242, 28
	v_lshl_add_u64 v[12:13], v[12:13], 0, v[18:19]
	s_add_i32 s6, s6, s7
	v_add_co_u32_e32 v14, vcc, 0x2000, v12
	v_lshl_or_b32 v18, s6, 4, v1
	s_nop 0
	v_addc_co_u32_e32 v15, vcc, 0, v13, vcc
	v_mad_i64_i32 v[70:71], vcc, v18, s33, v[70:71]
	v_lshl_add_u64 v[70:71], v[70:71], 0, s[84:85]
	v_mov_b32_e32 v147, v19
	v_lshl_add_u64 v[70:71], v[70:71], 0, v[146:147]
	s_mov_b64 vcc, 0x2000
	v_lshl_add_u64 v[72:73], v[70:71], 0, vcc
	v_add_co_u32_e32 v70, vcc, 0x2000, v70
	global_load_dwordx4 v[2:5], v[2:3], off offset:2048
	s_nop 0
	global_load_dwordx4 v[6:9], v[6:7], off offset:2048
	s_nop 0
	global_load_dwordx4 v[10:13], v[10:11], off offset:2048
	s_nop 0
	global_load_dwordx4 v[14:17], v[14:15], off offset:2048
	v_addc_co_u32_e32 v71, vcc, 0, v71, vcc
	global_load_dwordx2 v[126:127], v[72:73], off offset:32
	global_load_dwordx2 v[124:125], v[72:73], off offset:64
	global_load_dwordx2 v[122:123], v[72:73], off offset:96
	global_load_dwordx2 v[120:121], v[72:73], off offset:128
	global_load_dwordx2 v[134:135], v[70:71], off
	global_load_dwordx2 v[132:133], v[72:73], off offset:160
	global_load_dwordx2 v[130:131], v[72:73], off offset:192
	global_load_dwordx2 v[128:129], v[72:73], off offset:224
	s_and_saveexec_b64 vcc, s[0:1]
	s_cbranch_execz .LBB0_421
	s_lshl_b32 s6, s5, 1
	s_ashr_i32 s7, s6, 31
	v_lshl_add_u64 v[70:71], s[6:7], 2, v[112:113]
	global_load_dword v103, v[70:71], off sc1

.LBB0_423:
	ds_read_b128 v[158:161], v18
	ds_read_b128 v[162:165], v21
	s_add_i32 s5, s5, -1
	v_add_u32_e32 v18, 64, v18
	s_cmp_eq_u32 s5, 0
	s_waitcnt lgkmcnt(0)
	v_mfma_f32_16x16x32_bf16 v[98:101], v[162:165], v[158:161], v[98:101]
	ds_read_b128 v[162:165], v21 offset:4352
	s_waitcnt lgkmcnt(0)
	v_mfma_f32_16x16x32_bf16 v[94:97], v[162:165], v[158:161], v[94:97]
	ds_read_b128 v[162:165], v21 offset:8704
	s_waitcnt lgkmcnt(0)
	v_mfma_f32_16x16x32_bf16 v[90:93], v[162:165], v[158:161], v[90:93]
	ds_read_b128 v[162:165], v21 offset:13056
	s_waitcnt lgkmcnt(0)
	v_mfma_f32_16x16x32_bf16 v[86:89], v[162:165], v[158:161], v[86:89]
	ds_read_b128 v[162:165], v21 offset:17408
	s_waitcnt lgkmcnt(0)
	v_mfma_f32_16x16x32_bf16 v[82:85], v[162:165], v[158:161], v[82:85]
	ds_read_b128 v[162:165], v21 offset:21760
	s_waitcnt lgkmcnt(0)
	v_mfma_f32_16x16x32_bf16 v[78:81], v[162:165], v[158:161], v[78:81]
	ds_read_b128 v[162:165], v21 offset:26112
	s_waitcnt lgkmcnt(0)
	v_mfma_f32_16x16x32_bf16 v[74:77], v[162:165], v[158:161], v[74:77]
	ds_read_b128 v[162:165], v21 offset:30464
	v_add_u32_e32 v21, 64, v21
	s_waitcnt lgkmcnt(0)
	v_mfma_f32_16x16x32_bf16 v[70:73], v[162:165], v[158:161], v[70:73]
	s_cbranch_scc0 .LBB0_423
	v_lshlrev_b32_e32 v160, 16, v142
	s_lshl_b32 s5, s87, 4
	v_and_b32_e32 v161, 0xffff0000, v142
	v_fma_f32 v18, |v160|, s77, 1.0
	s_and_b32 s5, s5, 0xffffff80
	v_rcp_f32_e32 v162, v18
	v_fma_f32 v18, |v161|, s77, 1.0
	v_add_u32_e32 v144, s5, v150
	v_rcp_f32_e32 v163, v18
	v_ashrrev_i32_e32 v145, 31, v144
	v_lshlrev_b64 v[144:145], 12, v[144:145]
	v_pk_mul_f32 v[164:165], v[160:161], v[160:161]
	v_lshl_add_u64 v[158:159], s[74:75], 0, v[144:145]
	v_mul_f32_e32 v18, 0xbf38aa3b, v164
	v_mov_b64_e32 v[144:145], s[2:3]
	v_exp_f32_e32 v164, v18
	v_pk_fma_f32 v[166:167], v[162:163], s[76:77], v[144:145] op_sel_hi:[1,0,0]
	v_mul_f32_e32 v18, 0xbf38aa3b, v165
	v_pk_fma_f32 v[166:167], v[162:163], v[166:167], s[92:93] op_sel_hi:[1,1,0]
	v_exp_f32_e32 v165, v18
	v_pk_fma_f32 v[166:167], v[162:163], v[166:167], s[88:89] op_sel_hi:[1,1,0]
	v_cmp_gt_f32_e32 vcc, 0, v161
	v_pk_fma_f32 v[166:167], v[162:163], v[166:167], s[86:87] op_sel_hi:[1,1,0]
	v_lshlrev_b32_e32 v142, 16, v143
	v_pk_mul_f32 v[162:163], v[162:163], v[166:167]
	s_nop 0
	v_pk_add_f32 v[98:99], v[20:21], v[98:99] op_sel_hi:[0,1]
	v_pk_mul_f32 v[162:163], v[164:165], v[162:163]
	v_and_b32_e32 v143, 0xffff0000, v143
	v_pk_mul_f32 v[164:165], v[162:163], v[160:161]
	v_pk_fma_f32 v[162:163], v[162:163], v[160:161], v[160:161] neg_lo:[1,0,0] neg_hi:[1,0,0]
	v_fma_f32 v18, |v142|, s77, 1.0
	v_cndmask_b32_e32 v161, v163, v165, vcc
	v_cmp_gt_f32_e32 vcc, 0, v160
	v_pk_add_f32 v[100:101], v[20:21], v[100:101] op_sel_hi:[0,1]
	v_pk_add_f32 v[94:95], v[20:21], v[94:95] op_sel_hi:[0,1]
	v_cndmask_b32_e32 v160, v162, v164, vcc
	v_pk_mul_f32 v[98:99], v[98:99], v[160:161]
	v_rcp_f32_e32 v160, v18
	v_fma_f32 v18, |v143|, s77, 1.0
	v_rcp_f32_e32 v161, v18
	v_pk_mul_f32 v[162:163], v[142:143], v[142:143]
	v_cmp_gt_f32_e32 vcc, 0, v143
	v_mul_f32_e32 v18, 0xbf38aa3b, v162
	v_exp_f32_e32 v162, v18
	v_pk_fma_f32 v[164:165], v[160:161], s[76:77], v[144:145] op_sel_hi:[1,0,0]
	v_mul_f32_e32 v18, 0xbf38aa3b, v163
	v_pk_fma_f32 v[164:165], v[160:161], v[164:165], s[92:93] op_sel_hi:[1,1,0]
	v_exp_f32_e32 v163, v18
	v_pk_fma_f32 v[164:165], v[160:161], v[164:165], s[88:89] op_sel_hi:[1,1,0]
	v_lshl_or_b32 v18, s89, 8, v146
	v_pk_fma_f32 v[164:165], v[160:161], v[164:165], s[86:87] op_sel_hi:[1,1,0]
	v_pk_add_f32 v[96:97], v[20:21], v[96:97] op_sel_hi:[0,1]
	v_pk_mul_f32 v[160:161], v[160:161], v[164:165]
	v_pk_add_f32 v[90:91], v[20:21], v[90:91] op_sel_hi:[0,1]
	v_pk_mul_f32 v[160:161], v[162:163], v[160:161]
	v_pk_add_f32 v[92:93], v[20:21], v[92:93] op_sel_hi:[0,1]
	v_pk_mul_f32 v[162:163], v[160:161], v[142:143]
	v_pk_fma_f32 v[160:161], v[160:161], v[142:143], v[142:143] neg_lo:[1,0,0] neg_hi:[1,0,0]
	v_pk_add_f32 v[86:87], v[20:21], v[86:87] op_sel_hi:[0,1]
	v_cndmask_b32_e32 v143, v161, v163, vcc
	v_cmp_gt_f32_e32 vcc, 0, v142
	v_pk_add_f32 v[88:89], v[20:21], v[88:89] op_sel_hi:[0,1]
	v_pk_add_f32 v[82:83], v[20:21], v[82:83] op_sel_hi:[0,1]
	v_cndmask_b32_e32 v142, v160, v162, vcc
	v_pk_mul_f32 v[100:101], v[100:101], v[142:143]
	v_cvt_pk_bf16_f32 v142, v98, v99
	v_cvt_pk_bf16_f32 v143, v100, v101
	v_lshlrev_b32_e32 v100, 16, v140
	v_lshl_add_u64 v[98:99], v[158:159], 0, v[18:19]
	v_and_b32_e32 v101, 0xffff0000, v140
	v_fma_f32 v18, |v100|, s77, 1.0
	global_store_dwordx2 v[98:99], v[142:143], off offset:2048
	v_rcp_f32_e32 v142, v18
	v_fma_f32 v18, |v101|, s77, 1.0
	v_rcp_f32_e32 v143, v18
	v_pk_mul_f32 v[146:147], v[100:101], v[100:101]
	v_cmp_gt_f32_e32 vcc, 0, v101
	v_mul_f32_e32 v18, 0xbf38aa3b, v146
	v_exp_f32_e32 v146, v18
	v_pk_fma_f32 v[158:159], v[142:143], s[76:77], v[144:145] op_sel_hi:[1,0,0]
	v_mul_f32_e32 v18, 0xbf38aa3b, v147
	v_pk_fma_f32 v[158:159], v[142:143], v[158:159], s[92:93] op_sel_hi:[1,1,0]
	v_exp_f32_e32 v147, v18
	v_pk_fma_f32 v[158:159], v[142:143], v[158:159], s[88:89] op_sel_hi:[1,1,0]
	v_pk_add_f32 v[84:85], v[20:21], v[84:85] op_sel_hi:[0,1]
	v_pk_fma_f32 v[158:159], v[142:143], v[158:159], s[86:87] op_sel_hi:[1,1,0]
	v_pk_add_f32 v[78:79], v[20:21], v[78:79] op_sel_hi:[0,1]
	v_pk_mul_f32 v[142:143], v[142:143], v[158:159]
	v_pk_add_f32 v[80:81], v[20:21], v[80:81] op_sel_hi:[0,1]
	v_pk_mul_f32 v[142:143], v[146:147], v[142:143]
	v_pk_add_f32 v[74:75], v[20:21], v[74:75] op_sel_hi:[0,1]
	v_pk_mul_f32 v[146:147], v[142:143], v[100:101]
	v_pk_fma_f32 v[142:143], v[142:143], v[100:101], v[100:101] neg_lo:[1,0,0] neg_hi:[1,0,0]
	v_pk_add_f32 v[76:77], v[20:21], v[76:77] op_sel_hi:[0,1]
	v_cndmask_b32_e32 v101, v143, v147, vcc
	v_cmp_gt_f32_e32 vcc, 0, v100
	v_pk_add_f32 v[70:71], v[20:21], v[70:71] op_sel_hi:[0,1]
	v_pk_add_f32 v[72:73], v[20:21], v[72:73] op_sel_hi:[0,1]
	v_cndmask_b32_e32 v100, v142, v146, vcc
	v_pk_mul_f32 v[94:95], v[94:95], v[100:101]
	v_lshlrev_b32_e32 v100, 16, v141
	v_and_b32_e32 v101, 0xffff0000, v141
	v_fma_f32 v18, |v100|, s77, 1.0
	v_rcp_f32_e32 v140, v18
	v_fma_f32 v18, |v101|, s77, 1.0
	v_rcp_f32_e32 v141, v18
	v_pk_mul_f32 v[142:143], v[100:101], v[100:101]
	v_cmp_gt_f32_e32 vcc, 0, v101
	v_mul_f32_e32 v18, 0xbf38aa3b, v142
	v_exp_f32_e32 v142, v18
	v_pk_fma_f32 v[146:147], v[140:141], s[76:77], v[144:145] op_sel_hi:[1,0,0]
	v_mul_f32_e32 v18, 0xbf38aa3b, v143
	v_pk_fma_f32 v[146:147], v[140:141], v[146:147], s[92:93] op_sel_hi:[1,1,0]
	v_exp_f32_e32 v143, v18
	v_pk_fma_f32 v[146:147], v[140:141], v[146:147], s[88:89] op_sel_hi:[1,1,0]
	v_cvt_pk_bf16_f32 v94, v94, v95
	v_pk_fma_f32 v[146:147], v[140:141], v[146:147], s[86:87] op_sel_hi:[1,1,0]
	s_nop 0
	v_pk_mul_f32 v[140:141], v[140:141], v[146:147]
	s_nop 0
	v_pk_mul_f32 v[140:141], v[142:143], v[140:141]
	s_nop 0
	v_pk_mul_f32 v[142:143], v[140:141], v[100:101]
	v_pk_fma_f32 v[140:141], v[140:141], v[100:101], v[100:101] neg_lo:[1,0,0] neg_hi:[1,0,0]
	s_nop 0
	v_cndmask_b32_e32 v101, v141, v143, vcc
	v_cmp_gt_f32_e32 vcc, 0, v100
	s_nop 1
	v_cndmask_b32_e32 v100, v140, v142, vcc
	v_pk_mul_f32 v[96:97], v[96:97], v[100:101]
	v_cvt_pk_bf16_f32 v95, v96, v97
	global_store_dwordx2 v[98:99], v[94:95], off offset:2080
	v_lshlrev_b32_e32 v94, 16, v138
	v_and_b32_e32 v95, 0xffff0000, v138
	v_fma_f32 v18, |v94|, s77, 1.0
	v_rcp_f32_e32 v96, v18
	v_fma_f32 v18, |v95|, s77, 1.0
	v_rcp_f32_e32 v97, v18
	v_pk_mul_f32 v[100:101], v[94:95], v[94:95]
	v_cmp_gt_f32_e32 vcc, 0, v95
	v_mul_f32_e32 v18, 0xbf38aa3b, v100
	v_exp_f32_e32 v100, v18
	v_pk_fma_f32 v[140:141], v[96:97], s[76:77], v[144:145] op_sel_hi:[1,0,0]
	v_mul_f32_e32 v18, 0xbf38aa3b, v101
	v_pk_fma_f32 v[140:141], v[96:97], v[140:141], s[92:93] op_sel_hi:[1,1,0]
	v_exp_f32_e32 v101, v18
	v_pk_fma_f32 v[140:141], v[96:97], v[140:141], s[88:89] op_sel_hi:[1,1,0]
	s_nop 0
	v_pk_fma_f32 v[140:141], v[96:97], v[140:141], s[86:87] op_sel_hi:[1,1,0]
	s_nop 0
	v_pk_mul_f32 v[96:97], v[96:97], v[140:141]
	v_pk_mul_f32 v[96:97], v[100:101], v[96:97]
	s_nop 0
	v_pk_mul_f32 v[100:101], v[96:97], v[94:95]
	v_pk_fma_f32 v[96:97], v[96:97], v[94:95], v[94:95] neg_lo:[1,0,0] neg_hi:[1,0,0]
	s_nop 0
	v_cndmask_b32_e32 v95, v97, v101, vcc
	v_cmp_gt_f32_e32 vcc, 0, v94
	s_nop 1
	v_cndmask_b32_e32 v94, v96, v100, vcc
	v_pk_mul_f32 v[90:91], v[90:91], v[94:95]
	v_lshlrev_b32_e32 v94, 16, v139
	v_and_b32_e32 v95, 0xffff0000, v139
	v_fma_f32 v18, |v94|, s77, 1.0
	v_rcp_f32_e32 v96, v18
	v_fma_f32 v18, |v95|, s77, 1.0
	v_rcp_f32_e32 v97, v18
	v_pk_mul_f32 v[100:101], v[94:95], v[94:95]
	v_cmp_gt_f32_e32 vcc, 0, v95
	v_mul_f32_e32 v18, 0xbf38aa3b, v100
	v_exp_f32_e32 v100, v18
	v_pk_fma_f32 v[138:139], v[96:97], s[76:77], v[144:145] op_sel_hi:[1,0,0]
	v_mul_f32_e32 v18, 0xbf38aa3b, v101
	v_pk_fma_f32 v[138:139], v[96:97], v[138:139], s[92:93] op_sel_hi:[1,1,0]
	v_exp_f32_e32 v101, v18
	v_pk_fma_f32 v[138:139], v[96:97], v[138:139], s[88:89] op_sel_hi:[1,1,0]
	v_cvt_pk_bf16_f32 v90, v90, v91
	v_pk_fma_f32 v[138:139], v[96:97], v[138:139], s[86:87] op_sel_hi:[1,1,0]
	s_nop 0
	v_pk_mul_f32 v[96:97], v[96:97], v[138:139]
	v_pk_mul_f32 v[96:97], v[100:101], v[96:97]
	s_nop 0
	v_pk_mul_f32 v[100:101], v[96:97], v[94:95]
	v_pk_fma_f32 v[96:97], v[96:97], v[94:95], v[94:95] neg_lo:[1,0,0] neg_hi:[1,0,0]
	s_nop 0
	v_cndmask_b32_e32 v95, v97, v101, vcc
	v_cmp_gt_f32_e32 vcc, 0, v94
	s_nop 1
	v_cndmask_b32_e32 v94, v96, v100, vcc
	v_pk_mul_f32 v[92:93], v[92:93], v[94:95]
	s_nop 0
	v_cvt_pk_bf16_f32 v91, v92, v93
	global_store_dwordx2 v[98:99], v[90:91], off offset:2112
	v_lshlrev_b32_e32 v90, 16, v136
	v_and_b32_e32 v91, 0xffff0000, v136
	v_fma_f32 v18, |v90|, s77, 1.0
	v_rcp_f32_e32 v92, v18
	v_fma_f32 v18, |v91|, s77, 1.0
	v_rcp_f32_e32 v93, v18
	v_pk_mul_f32 v[94:95], v[90:91], v[90:91]
	v_cmp_gt_f32_e32 vcc, 0, v91
	v_mul_f32_e32 v18, 0xbf38aa3b, v94
	v_exp_f32_e32 v94, v18
	v_pk_fma_f32 v[96:97], v[92:93], s[76:77], v[144:145] op_sel_hi:[1,0,0]
	v_mul_f32_e32 v18, 0xbf38aa3b, v95
	v_pk_fma_f32 v[96:97], v[92:93], v[96:97], s[92:93] op_sel_hi:[1,1,0]
	v_exp_f32_e32 v95, v18
	v_pk_fma_f32 v[96:97], v[92:93], v[96:97], s[88:89] op_sel_hi:[1,1,0]
	s_nop 0
	v_pk_fma_f32 v[96:97], v[92:93], v[96:97], s[86:87] op_sel_hi:[1,1,0]
	s_nop 0
	v_pk_mul_f32 v[92:93], v[92:93], v[96:97]
	s_nop 0
	v_pk_mul_f32 v[92:93], v[94:95], v[92:93]
	s_nop 0
	v_pk_mul_f32 v[94:95], v[92:93], v[90:91]
	v_pk_fma_f32 v[92:93], v[92:93], v[90:91], v[90:91] neg_lo:[1,0,0] neg_hi:[1,0,0]
	s_nop 0
	v_cndmask_b32_e32 v91, v93, v95, vcc
	v_cmp_gt_f32_e32 vcc, 0, v90
	s_nop 1
	v_cndmask_b32_e32 v90, v92, v94, vcc
	v_pk_mul_f32 v[86:87], v[86:87], v[90:91]
	v_lshlrev_b32_e32 v90, 16, v137
	v_and_b32_e32 v91, 0xffff0000, v137
	v_fma_f32 v18, |v90|, s77, 1.0
	v_rcp_f32_e32 v92, v18
	v_fma_f32 v18, |v91|, s77, 1.0
	v_rcp_f32_e32 v93, v18
	v_pk_mul_f32 v[94:95], v[90:91], v[90:91]
	v_cmp_gt_f32_e32 vcc, 0, v91
	v_mul_f32_e32 v18, 0xbf38aa3b, v94
	v_exp_f32_e32 v94, v18
	v_pk_fma_f32 v[96:97], v[92:93], s[76:77], v[144:145] op_sel_hi:[1,0,0]
	v_mul_f32_e32 v18, 0xbf38aa3b, v95
	v_pk_fma_f32 v[96:97], v[92:93], v[96:97], s[92:93] op_sel_hi:[1,1,0]
	v_exp_f32_e32 v95, v18
	v_pk_fma_f32 v[96:97], v[92:93], v[96:97], s[88:89] op_sel_hi:[1,1,0]
	v_cvt_pk_bf16_f32 v86, v86, v87
	v_pk_fma_f32 v[96:97], v[92:93], v[96:97], s[86:87] op_sel_hi:[1,1,0]
	v_pk_mul_f32 v[92:93], v[92:93], v[96:97]
	s_nop 0
	v_pk_mul_f32 v[92:93], v[94:95], v[92:93]
	s_nop 0
	v_pk_mul_f32 v[94:95], v[92:93], v[90:91]
	v_pk_fma_f32 v[92:93], v[92:93], v[90:91], v[90:91] neg_lo:[1,0,0] neg_hi:[1,0,0]
	s_nop 0
	v_cndmask_b32_e32 v91, v93, v95, vcc
	v_cmp_gt_f32_e32 vcc, 0, v90
	s_nop 1
	v_cndmask_b32_e32 v90, v92, v94, vcc
	v_pk_mul_f32 v[88:89], v[88:89], v[90:91]
	s_nop 0
	v_cvt_pk_bf16_f32 v87, v88, v89
	global_store_dwordx2 v[98:99], v[86:87], off offset:2144
	v_lshlrev_b32_e32 v86, 16, v118
	v_and_b32_e32 v87, 0xffff0000, v118
	v_fma_f32 v18, |v86|, s77, 1.0
	v_rcp_f32_e32 v88, v18
	v_fma_f32 v18, |v87|, s77, 1.0
	v_rcp_f32_e32 v89, v18
	v_pk_mul_f32 v[90:91], v[86:87], v[86:87]
	v_cmp_gt_f32_e32 vcc, 0, v87
	v_mul_f32_e32 v18, 0xbf38aa3b, v90
	v_exp_f32_e32 v90, v18
	v_pk_fma_f32 v[92:93], v[88:89], s[76:77], v[144:145] op_sel_hi:[1,0,0]
	v_mul_f32_e32 v18, 0xbf38aa3b, v91
	v_pk_fma_f32 v[92:93], v[88:89], v[92:93], s[92:93] op_sel_hi:[1,1,0]
	v_exp_f32_e32 v91, v18
	v_pk_fma_f32 v[92:93], v[88:89], v[92:93], s[88:89] op_sel_hi:[1,1,0]
	s_nop 0
	v_pk_fma_f32 v[92:93], v[88:89], v[92:93], s[86:87] op_sel_hi:[1,1,0]
	s_nop 0
	v_pk_mul_f32 v[88:89], v[88:89], v[92:93]
	s_nop 0
	v_pk_mul_f32 v[88:89], v[90:91], v[88:89]
	s_nop 0
	v_pk_mul_f32 v[90:91], v[88:89], v[86:87]
	v_pk_fma_f32 v[88:89], v[88:89], v[86:87], v[86:87] neg_lo:[1,0,0] neg_hi:[1,0,0]
	s_nop 0
	v_cndmask_b32_e32 v87, v89, v91, vcc
	v_cmp_gt_f32_e32 vcc, 0, v86
	s_nop 1
	v_cndmask_b32_e32 v86, v88, v90, vcc
	v_pk_mul_f32 v[82:83], v[82:83], v[86:87]
	v_lshlrev_b32_e32 v86, 16, v119
	v_and_b32_e32 v87, 0xffff0000, v119
	v_fma_f32 v18, |v86|, s77, 1.0
	v_rcp_f32_e32 v88, v18
	v_fma_f32 v18, |v87|, s77, 1.0
	v_rcp_f32_e32 v89, v18
	v_pk_mul_f32 v[90:91], v[86:87], v[86:87]
	v_cmp_gt_f32_e32 vcc, 0, v87
	v_mul_f32_e32 v18, 0xbf38aa3b, v90
	v_exp_f32_e32 v90, v18
	v_pk_fma_f32 v[92:93], v[88:89], s[76:77], v[144:145] op_sel_hi:[1,0,0]
	v_mul_f32_e32 v18, 0xbf38aa3b, v91
	v_pk_fma_f32 v[92:93], v[88:89], v[92:93], s[92:93] op_sel_hi:[1,1,0]
	v_exp_f32_e32 v91, v18
	v_pk_fma_f32 v[92:93], v[88:89], v[92:93], s[88:89] op_sel_hi:[1,1,0]
	v_cvt_pk_bf16_f32 v82, v82, v83
	v_pk_fma_f32 v[92:93], v[88:89], v[92:93], s[86:87] op_sel_hi:[1,1,0]
	v_pk_mul_f32 v[88:89], v[88:89], v[92:93]
	s_nop 0
	v_pk_mul_f32 v[88:89], v[90:91], v[88:89]
	s_nop 0
	v_pk_mul_f32 v[90:91], v[88:89], v[86:87]
	v_pk_fma_f32 v[88:89], v[88:89], v[86:87], v[86:87] neg_lo:[1,0,0] neg_hi:[1,0,0]
	s_nop 0
	v_cndmask_b32_e32 v87, v89, v91, vcc
	v_cmp_gt_f32_e32 vcc, 0, v86
	s_nop 1
	v_cndmask_b32_e32 v86, v88, v90, vcc
	v_pk_mul_f32 v[84:85], v[84:85], v[86:87]
	s_nop 0
	v_cvt_pk_bf16_f32 v83, v84, v85
	global_store_dwordx2 v[98:99], v[82:83], off offset:2176
	v_lshlrev_b32_e32 v82, 16, v116
	v_and_b32_e32 v83, 0xffff0000, v116
	v_fma_f32 v18, |v82|, s77, 1.0
	v_rcp_f32_e32 v84, v18
	v_fma_f32 v18, |v83|, s77, 1.0
	v_rcp_f32_e32 v85, v18
	v_pk_mul_f32 v[86:87], v[82:83], v[82:83]
	v_cmp_gt_f32_e32 vcc, 0, v83
	v_mul_f32_e32 v18, 0xbf38aa3b, v86
	v_exp_f32_e32 v86, v18
	v_pk_fma_f32 v[88:89], v[84:85], s[76:77], v[144:145] op_sel_hi:[1,0,0]
	v_mul_f32_e32 v18, 0xbf38aa3b, v87
	v_pk_fma_f32 v[88:89], v[84:85], v[88:89], s[92:93] op_sel_hi:[1,1,0]
	v_exp_f32_e32 v87, v18
	v_pk_fma_f32 v[88:89], v[84:85], v[88:89], s[88:89] op_sel_hi:[1,1,0]
	s_nop 0
	v_pk_fma_f32 v[88:89], v[84:85], v[88:89], s[86:87] op_sel_hi:[1,1,0]
	s_nop 0
	v_pk_mul_f32 v[84:85], v[84:85], v[88:89]
	s_nop 0
	v_pk_mul_f32 v[84:85], v[86:87], v[84:85]
	s_nop 0
	v_pk_mul_f32 v[86:87], v[84:85], v[82:83]
	v_pk_fma_f32 v[84:85], v[84:85], v[82:83], v[82:83] neg_lo:[1,0,0] neg_hi:[1,0,0]
	s_nop 0
	v_cndmask_b32_e32 v83, v85, v87, vcc
	v_cmp_gt_f32_e32 vcc, 0, v82
	s_nop 1
	v_cndmask_b32_e32 v82, v84, v86, vcc
	v_pk_mul_f32 v[78:79], v[78:79], v[82:83]
	v_lshlrev_b32_e32 v82, 16, v117
	v_and_b32_e32 v83, 0xffff0000, v117
	v_fma_f32 v18, |v82|, s77, 1.0
	v_rcp_f32_e32 v84, v18
	v_fma_f32 v18, |v83|, s77, 1.0
	v_rcp_f32_e32 v85, v18
	v_pk_mul_f32 v[86:87], v[82:83], v[82:83]
	v_cmp_gt_f32_e32 vcc, 0, v83
	v_mul_f32_e32 v18, 0xbf38aa3b, v86
	v_exp_f32_e32 v86, v18
	v_pk_fma_f32 v[88:89], v[84:85], s[76:77], v[144:145] op_sel_hi:[1,0,0]
	v_mul_f32_e32 v18, 0xbf38aa3b, v87
	v_pk_fma_f32 v[88:89], v[84:85], v[88:89], s[92:93] op_sel_hi:[1,1,0]
	v_exp_f32_e32 v87, v18
	v_pk_fma_f32 v[88:89], v[84:85], v[88:89], s[88:89] op_sel_hi:[1,1,0]
	v_cvt_pk_bf16_f32 v78, v78, v79
	v_pk_fma_f32 v[88:89], v[84:85], v[88:89], s[86:87] op_sel_hi:[1,1,0]
	v_pk_mul_f32 v[84:85], v[84:85], v[88:89]
	s_nop 0
	v_pk_mul_f32 v[84:85], v[86:87], v[84:85]
	s_nop 0
	v_pk_mul_f32 v[86:87], v[84:85], v[82:83]
	v_pk_fma_f32 v[84:85], v[84:85], v[82:83], v[82:83] neg_lo:[1,0,0] neg_hi:[1,0,0]
	s_nop 0
	v_cndmask_b32_e32 v83, v85, v87, vcc
	v_cmp_gt_f32_e32 vcc, 0, v82
	s_nop 1
	v_cndmask_b32_e32 v82, v84, v86, vcc
	v_pk_mul_f32 v[80:81], v[80:81], v[82:83]
	s_nop 0
	v_cvt_pk_bf16_f32 v79, v80, v81
	global_store_dwordx2 v[98:99], v[78:79], off offset:2208
	v_lshlrev_b32_e32 v78, 16, v114
	v_and_b32_e32 v79, 0xffff0000, v114
	v_fma_f32 v18, |v78|, s77, 1.0
	v_rcp_f32_e32 v80, v18
	v_fma_f32 v18, |v79|, s77, 1.0
	v_rcp_f32_e32 v81, v18
	v_pk_mul_f32 v[82:83], v[78:79], v[78:79]
	v_cmp_gt_f32_e32 vcc, 0, v79
	v_mul_f32_e32 v18, 0xbf38aa3b, v82
	v_exp_f32_e32 v82, v18
	v_pk_fma_f32 v[84:85], v[80:81], s[76:77], v[144:145] op_sel_hi:[1,0,0]
	v_mul_f32_e32 v18, 0xbf38aa3b, v83
	v_pk_fma_f32 v[84:85], v[80:81], v[84:85], s[92:93] op_sel_hi:[1,1,0]
	v_exp_f32_e32 v83, v18
	v_pk_fma_f32 v[84:85], v[80:81], v[84:85], s[88:89] op_sel_hi:[1,1,0]
	s_nop 0
	v_pk_fma_f32 v[84:85], v[80:81], v[84:85], s[86:87] op_sel_hi:[1,1,0]
	s_nop 0
	v_pk_mul_f32 v[80:81], v[80:81], v[84:85]
	s_nop 0
	v_pk_mul_f32 v[80:81], v[82:83], v[80:81]
	s_nop 0
	v_pk_mul_f32 v[82:83], v[80:81], v[78:79]
	v_pk_fma_f32 v[80:81], v[80:81], v[78:79], v[78:79] neg_lo:[1,0,0] neg_hi:[1,0,0]
	s_nop 0
	v_cndmask_b32_e32 v79, v81, v83, vcc
	v_cmp_gt_f32_e32 vcc, 0, v78
	s_nop 1
	v_cndmask_b32_e32 v78, v80, v82, vcc
	v_pk_mul_f32 v[74:75], v[74:75], v[78:79]
	v_lshlrev_b32_e32 v78, 16, v115
	v_and_b32_e32 v79, 0xffff0000, v115
	v_fma_f32 v18, |v78|, s77, 1.0
	v_rcp_f32_e32 v80, v18
	v_fma_f32 v18, |v79|, s77, 1.0
	v_rcp_f32_e32 v81, v18
	v_pk_mul_f32 v[82:83], v[78:79], v[78:79]
	v_cmp_gt_f32_e32 vcc, 0, v79
	v_mul_f32_e32 v18, 0xbf38aa3b, v82
	v_exp_f32_e32 v82, v18
	v_pk_fma_f32 v[84:85], v[80:81], s[76:77], v[144:145] op_sel_hi:[1,0,0]
	v_mul_f32_e32 v18, 0xbf38aa3b, v83
	v_pk_fma_f32 v[84:85], v[80:81], v[84:85], s[92:93] op_sel_hi:[1,1,0]
	v_exp_f32_e32 v83, v18
	v_pk_fma_f32 v[84:85], v[80:81], v[84:85], s[88:89] op_sel_hi:[1,1,0]
	v_cvt_pk_bf16_f32 v74, v74, v75
	v_pk_fma_f32 v[84:85], v[80:81], v[84:85], s[86:87] op_sel_hi:[1,1,0]
	v_pk_mul_f32 v[80:81], v[80:81], v[84:85]
	s_nop 0
	v_pk_mul_f32 v[80:81], v[82:83], v[80:81]
	s_nop 0
	v_pk_mul_f32 v[82:83], v[80:81], v[78:79]
	v_pk_fma_f32 v[80:81], v[80:81], v[78:79], v[78:79] neg_lo:[1,0,0] neg_hi:[1,0,0]
	s_nop 0
	v_cndmask_b32_e32 v79, v81, v83, vcc
	v_cmp_gt_f32_e32 vcc, 0, v78
	s_nop 1
	v_cndmask_b32_e32 v78, v80, v82, vcc
	v_pk_mul_f32 v[76:77], v[76:77], v[78:79]
	s_nop 0
	v_cvt_pk_bf16_f32 v75, v76, v77
	global_store_dwordx2 v[98:99], v[74:75], off offset:2240
	v_lshlrev_b32_e32 v74, 16, v104
	v_and_b32_e32 v75, 0xffff0000, v104
	v_fma_f32 v18, |v74|, s77, 1.0
	v_rcp_f32_e32 v76, v18
	v_fma_f32 v18, |v75|, s77, 1.0
	v_rcp_f32_e32 v77, v18
	v_pk_mul_f32 v[78:79], v[74:75], v[74:75]
	v_cmp_gt_f32_e32 vcc, 0, v75
	v_mul_f32_e32 v18, 0xbf38aa3b, v78
	v_exp_f32_e32 v78, v18
	v_pk_fma_f32 v[80:81], v[76:77], s[76:77], v[144:145] op_sel_hi:[1,0,0]
	v_mul_f32_e32 v18, 0xbf38aa3b, v79
	v_pk_fma_f32 v[80:81], v[76:77], v[80:81], s[92:93] op_sel_hi:[1,1,0]
	v_exp_f32_e32 v79, v18
	v_pk_fma_f32 v[80:81], v[76:77], v[80:81], s[88:89] op_sel_hi:[1,1,0]
	s_nop 0
	v_pk_fma_f32 v[80:81], v[76:77], v[80:81], s[86:87] op_sel_hi:[1,1,0]
	s_nop 0
	v_pk_mul_f32 v[76:77], v[76:77], v[80:81]
	s_nop 0
	v_pk_mul_f32 v[76:77], v[78:79], v[76:77]
	s_nop 0
	v_pk_mul_f32 v[78:79], v[76:77], v[74:75]
	v_pk_fma_f32 v[76:77], v[76:77], v[74:75], v[74:75] neg_lo:[1,0,0] neg_hi:[1,0,0]
	s_nop 0
	v_cndmask_b32_e32 v75, v77, v79, vcc
	v_cmp_gt_f32_e32 vcc, 0, v74
	s_nop 1
	v_cndmask_b32_e32 v74, v76, v78, vcc
	v_pk_mul_f32 v[70:71], v[70:71], v[74:75]
	v_lshlrev_b32_e32 v74, 16, v105
	v_and_b32_e32 v75, 0xffff0000, v105
	v_fma_f32 v18, |v74|, s77, 1.0
	v_rcp_f32_e32 v76, v18
	v_fma_f32 v18, |v75|, s77, 1.0
	v_rcp_f32_e32 v77, v18
	v_pk_mul_f32 v[78:79], v[74:75], v[74:75]
	v_cmp_gt_f32_e32 vcc, 0, v75
	v_mul_f32_e32 v18, 0xbf38aa3b, v78
	v_exp_f32_e32 v78, v18
	v_pk_fma_f32 v[80:81], v[76:77], s[76:77], v[144:145] op_sel_hi:[1,0,0]
	v_mul_f32_e32 v18, 0xbf38aa3b, v79
	v_pk_fma_f32 v[80:81], v[76:77], v[80:81], s[92:93] op_sel_hi:[1,1,0]
	v_exp_f32_e32 v79, v18
	v_pk_fma_f32 v[80:81], v[76:77], v[80:81], s[88:89] op_sel_hi:[1,1,0]
	v_cvt_pk_bf16_f32 v70, v70, v71
	v_pk_fma_f32 v[80:81], v[76:77], v[80:81], s[86:87] op_sel_hi:[1,1,0]
	v_pk_mul_f32 v[76:77], v[76:77], v[80:81]
	s_mov_b32 s87, s4
	v_pk_mul_f32 v[76:77], v[78:79], v[76:77]
	s_nop 0
	v_pk_mul_f32 v[78:79], v[76:77], v[74:75]
	v_pk_fma_f32 v[76:77], v[76:77], v[74:75], v[74:75] neg_lo:[1,0,0] neg_hi:[1,0,0]
	s_nop 0
	v_cndmask_b32_e32 v75, v77, v79, vcc
	v_cmp_gt_f32_e32 vcc, 0, v74
	s_nop 1
	v_cndmask_b32_e32 v74, v76, v78, vcc
	v_pk_mul_f32 v[72:73], v[72:73], v[74:75]
	s_and_b64 vcc, exec, s[68:69]
	v_cvt_pk_bf16_f32 v71, v72, v73
	global_store_dwordx2 v[98:99], v[70:71], off offset:2272
	s_waitcnt vmcnt(8)
	v_mov_b64_e32 v[142:143], v[134:135]
	v_mov_b64_e32 v[140:141], v[126:127]
	v_mov_b64_e32 v[138:139], v[124:125]
	v_mov_b64_e32 v[136:137], v[122:123]
	v_mov_b64_e32 v[118:119], v[120:121]
	v_mov_b64_e32 v[116:117], v[132:133]
	v_mov_b64_e32 v[114:115], v[130:131]
	v_mov_b64_e32 v[104:105], v[128:129]
	s_barrier
	s_cbranch_vccz .LBB0_412
	v_readlane_b32 s87, v242, 63
	v_readlane_b32 s85, v242, 43
	v_readlane_b32 s86, v242, 42
	v_readlane_b32 s88, v242, 41
	v_readlane_b32 s89, v242, 40
	v_readlane_b32 s92, v242, 44

.LBB0_1354:
	v_lshl_add_u32 v52, s60, 8, v218
	v_ashrrev_i32_e32 v53, 31, v52
	v_lshl_add_u64 v[50:51], v[52:53], 2, s[12:13]
	global_load_dword v57, v[50:51], off
	s_lshl_b32 s2, s18, 8
	s_ashr_i32 s3, s2, 31
	v_lshlrev_b64 v[2:3], 11, v[52:53]
	v_lshl_add_u64 v[58:59], v[2:3], 0, s[2:3]
	v_or_b32_e32 v58, v58, v194
	v_lshlrev_b64 v[2:3], 1, v[58:59]
	v_lshl_add_u64 v[64:65], s[10:11], 0, v[2:3]
	global_load_dwordx4 v[214:217], v[64:65], off
	v_lshl_add_u64 v[62:63], s[14:15], 0, v[2:3]
	global_load_dwordx4 v[224:227], v[62:63], off
	v_and_b32_e32 v5, 64, v199
	v_xor_b32_e32 v4, 16, v199
	v_add_u32_e32 v205, 64, v5
	v_cmp_lt_i32_e32 vcc, v4, v205
	v_or_b32_e32 v2, 0x100, v2
	global_load_dword v56, v[50:51], off offset:64
	global_load_dword v55, v[50:51], off offset:128
	global_load_dword v54, v[50:51], off offset:192
	v_cndmask_b32_e32 v4, v199, v4, vcc
	v_add_co_u32_e32 v6, vcc, s76, v64
	v_lshlrev_b32_e32 v201, 2, v4
	s_nop 0
	v_addc_co_u32_e32 v7, vcc, 0, v65, vcc
	v_add_co_u32_e32 v8, vcc, s76, v62
	v_lshl_add_u64 v[4:5], s[10:11], 0, v[2:3]
	s_nop 0
	v_addc_co_u32_e32 v9, vcc, 0, v63, vcc
	v_add_co_u32_e32 v10, vcc, s77, v64
	v_lshl_add_u64 v[2:3], s[14:15], 0, v[2:3]
	s_nop 0
	v_addc_co_u32_e32 v11, vcc, 0, v65, vcc
	v_add_co_u32_e32 v12, vcc, s77, v62
	s_nop 1
	v_addc_co_u32_e32 v13, vcc, 0, v63, vcc
	v_add_co_u32_e32 v14, vcc, s84, v64
	s_nop 1
	v_addc_co_u32_e32 v15, vcc, 0, v65, vcc
	v_add_co_u32_e32 v60, vcc, s84, v62
	s_nop 1
	v_addc_co_u32_e32 v61, vcc, 0, v63, vcc
	global_load_dwordx4 v[228:231], v[4:5], off
	global_load_dwordx4 v[232:235], v[2:3], off
	global_load_dwordx4 v[46:49], v[6:7], off
	global_load_dwordx4 v[38:41], v[6:7], off offset:256
	global_load_dwordx4 v[42:45], v[8:9], off
	global_load_dwordx4 v[34:37], v[8:9], off offset:256
	global_load_dwordx4 v[30:33], v[10:11], off
	global_load_dwordx4 v[22:25], v[10:11], off offset:256
	global_load_dwordx4 v[26:29], v[12:13], off
	global_load_dwordx4 v[18:21], v[12:13], off offset:256
	s_nop 0
	global_load_dwordx4 v[10:13], v[14:15], off
	global_load_dwordx4 v[6:9], v[14:15], off offset:256
	s_nop 0
	global_load_dwordx4 v[14:17], v[60:61], off
	global_load_dwordx4 v[2:5], v[60:61], off offset:256
	s_waitcnt vmcnt(14)
	v_mul_f32_e32 v57, 0x39800000, v57
	s_nop 0
	v_mul_f32_e32 v68, v68, v57
	v_mul_f32_e32 v69, v69, v57
	v_mul_f32_e32 v60, v66, v57
	v_mul_f32_e32 v61, v126, v57
	v_mul_f32_e32 v66, v67, v57
	v_mul_f32_e32 v67, v127, v57
	v_mul_f32_e32 v61, 0xbfb8aa3b, v61
	v_mul_f32_e32 v67, 0xbfb8aa3b, v67
	v_mul_f32_e32 v68, 0xbfb8aa3b, v68
	v_mul_f32_e32 v128, v128, v57
	v_mul_f32_e32 v69, 0xbfb8aa3b, v69
	v_mul_f32_e32 v129, v129, v57
	v_mul_f32_e32 v60, 0xbfb8aa3b, v60
	v_mul_f32_e32 v66, 0xbfb8aa3b, v66
	v_exp_f32_e32 v221, v61
	v_exp_f32_e32 v237, v67
	v_exp_f32_e32 v68, v68
	v_mul_f32_e32 v128, 0xbfb8aa3b, v128
	v_exp_f32_e32 v69, v69
	v_mul_f32_e32 v129, 0xbfb8aa3b, v129
	v_mul_f32_e32 v98, v98, v57
	v_mul_f32_e32 v99, v99, v57
	v_exp_f32_e32 v211, v60
	v_exp_f32_e32 v223, v66
	v_exp_f32_e32 v128, v128
	v_exp_f32_e32 v129, v129
	v_mul_f32_e32 v98, 0xbfb8aa3b, v98
	v_mul_f32_e32 v94, v94, v57
	v_mul_f32_e32 v99, 0xbfb8aa3b, v99
	v_mul_f32_e32 v95, v95, v57
	v_exp_f32_e32 v98, v98
	v_mul_f32_e32 v94, 0xbfb8aa3b, v94
	v_exp_f32_e32 v99, v99
	v_mul_f32_e32 v95, 0xbfb8aa3b, v95
	v_mul_f32_e32 v100, v100, v57
	v_mul_f32_e32 v101, v101, v57
	v_exp_f32_e32 v94, v94
	v_exp_f32_e32 v95, v95
	v_mul_f32_e32 v100, 0xbfb8aa3b, v100
	v_mul_f32_e32 v96, v96, v57
	v_mul_f32_e32 v101, 0xbfb8aa3b, v101
	v_mul_f32_e32 v57, v97, v57
	v_lshlrev_b32_e32 v60, 16, v214
	v_and_b32_e32 v61, 0xffff0000, v214
	v_add_f32_e32 v214, 1.0, v221
	v_add_f32_e32 v221, 1.0, v237
	v_add_f32_e32 v68, 1.0, v68
	v_add_f32_e32 v69, 1.0, v69
	v_exp_f32_e32 v100, v100
	v_mul_f32_e32 v96, 0xbfb8aa3b, v96
	v_exp_f32_e32 v101, v101
	v_mul_f32_e32 v57, 0xbfb8aa3b, v57
	v_lshlrev_b32_e32 v126, 16, v216
	v_and_b32_e32 v127, 0xffff0000, v216
	v_add_f32_e32 v211, 1.0, v211
	v_add_f32_e32 v216, 1.0, v223
	v_rcp_f32_e32 v240, v214
	v_rcp_f32_e32 v241, v221
	v_rcp_f32_e32 v68, v68
	v_add_f32_e32 v128, 1.0, v128
	v_rcp_f32_e32 v69, v69
	v_add_f32_e32 v129, 1.0, v129
	v_exp_f32_e32 v96, v96
	v_exp_f32_e32 v57, v57
	v_rcp_f32_e32 v238, v211
	v_rcp_f32_e32 v239, v216
	v_rcp_f32_e32 v128, v128
	v_rcp_f32_e32 v129, v129
	v_add_f32_e32 v98, 1.0, v98
	v_add_f32_e32 v99, 1.0, v99
	v_rcp_f32_e32 v98, v98
	v_add_f32_e32 v94, 1.0, v94
	v_rcp_f32_e32 v99, v99
	v_add_f32_e32 v95, 1.0, v95
	v_lshlrev_b32_e32 v66, 16, v224
	v_and_b32_e32 v67, 0xffff0000, v224
	v_lshlrev_b32_e32 v236, 16, v226
	v_and_b32_e32 v237, 0xffff0000, v226
	v_lshlrev_b32_e32 v214, 16, v215
	v_and_b32_e32 v215, 0xffff0000, v215
	v_lshlrev_b32_e32 v224, 16, v225
	v_and_b32_e32 v225, 0xffff0000, v225
	v_rcp_f32_e32 v94, v94
	v_rcp_f32_e32 v95, v95
	v_add_f32_e32 v100, 1.0, v100
	v_add_f32_e32 v101, 1.0, v101
	v_pk_fma_f32 v[126:127], v[240:241], v[236:237], v[126:127]
	v_pk_fma_f32 v[68:69], v[68:69], v[224:225], v[214:215]
	v_lshlrev_b32_e32 v214, 16, v217
	v_and_b32_e32 v215, 0xffff0000, v217
	v_lshlrev_b32_e32 v216, 16, v227
	v_and_b32_e32 v217, 0xffff0000, v227
	v_rcp_f32_e32 v100, v100
	v_add_f32_e32 v96, 1.0, v96
	v_rcp_f32_e32 v101, v101
	v_add_f32_e32 v57, 1.0, v57
	v_pk_fma_f32 v[66:67], v[238:239], v[66:67], v[60:61]
	v_pk_mul_f32 v[60:61], v[126:127], v[126:127]
	v_pk_fma_f32 v[128:129], v[128:129], v[216:217], v[214:215]
	s_waitcnt vmcnt(13)
	v_lshlrev_b32_e32 v216, 16, v228
	v_and_b32_e32 v217, 0xffff0000, v228
	s_waitcnt vmcnt(12)
	v_lshlrev_b32_e32 v224, 16, v232
	v_and_b32_e32 v225, 0xffff0000, v232
	v_rcp_f32_e32 v96, v96
	v_rcp_f32_e32 v97, v57
	v_pk_fma_f32 v[60:61], v[66:67], v[66:67], v[60:61]
	v_pk_mul_f32 v[214:215], v[128:129], v[128:129]
	v_pk_fma_f32 v[98:99], v[98:99], v[224:225], v[216:217]
	v_lshlrev_b32_e32 v216, 16, v230
	v_and_b32_e32 v217, 0xffff0000, v230
	v_lshlrev_b32_e32 v224, 16, v234
	v_and_b32_e32 v225, 0xffff0000, v234
	v_pk_fma_f32 v[214:215], v[68:69], v[68:69], v[214:215]
	v_pk_fma_f32 v[94:95], v[94:95], v[224:225], v[216:217]
	v_lshlrev_b32_e32 v224, 16, v229
	v_and_b32_e32 v225, 0xffff0000, v229
	v_lshlrev_b32_e32 v226, 16, v233
	v_and_b32_e32 v227, 0xffff0000, v233
	v_add_f32_e32 v57, v60, v61
	v_pk_mul_f32 v[216:217], v[94:95], v[94:95]
	v_pk_fma_f32 v[100:101], v[100:101], v[226:227], v[224:225]
	v_lshlrev_b32_e32 v224, 16, v231
	v_and_b32_e32 v225, 0xffff0000, v231
	v_lshlrev_b32_e32 v226, 16, v235
	v_and_b32_e32 v227, 0xffff0000, v235
	v_add_f32_e32 v57, v214, v57
	v_pk_fma_f32 v[216:217], v[98:99], v[98:99], v[216:217]
	v_pk_fma_f32 v[96:97], v[96:97], v[226:227], v[224:225]
	v_add_f32_e32 v57, v215, v57
	v_pk_mul_f32 v[224:225], v[96:97], v[96:97]
	v_add_f32_e32 v57, v216, v57
	v_pk_fma_f32 v[224:225], v[100:101], v[100:101], v[224:225]
	v_add_f32_e32 v57, v217, v57
	v_add_f32_e32 v57, v224, v57
	v_add_f32_e32 v57, v225, v57
	ds_bpermute_b32 v60, v201, v57
	v_xor_b32_e32 v61, 32, v199
	v_cmp_lt_i32_e32 vcc, v61, v205
	s_waitcnt lgkmcnt(0)
	v_add_f32_e32 v57, v57, v60
	v_cndmask_b32_e32 v61, v199, v61, vcc
	v_lshlrev_b32_e32 v205, 2, v61
	ds_bpermute_b32 v211, v205, v57
	v_lshl_add_u64 v[60:61], v[52:53], 2, s[16:17]
	s_and_saveexec_b64 s[6:7], s[0:1]
	s_cbranch_execz .LBB0_1356
	s_waitcnt lgkmcnt(0)
	v_add_f32_e32 v52, v57, v211
	global_atomic_add_f32 v[60:61], v52, off

.LBB0_1362:
	s_or_b64 exec, exec, s[6:7]
	global_load_dword v216, v[50:51], off offset:512
	v_add_co_u32_e32 v2, vcc, 0x80000, v64
	s_waitcnt lgkmcnt(0)
	s_nop 0
	v_addc_co_u32_e32 v3, vcc, 0, v65, vcc
	global_load_dwordx4 v[224:227], v[2:3], off
	v_add_co_u32_e32 v4, vcc, 0x80000, v62
	s_nop 1
	v_addc_co_u32_e32 v5, vcc, 0, v63, vcc
	global_load_dwordx4 v[228:231], v[4:5], off
	global_load_dword v215, v[50:51], off offset:576
	global_load_dword v214, v[50:51], off offset:640
	global_load_dword v211, v[50:51], off offset:704
	s_nop 0
	global_load_dwordx4 v[50:53], v[2:3], off offset:256
	global_load_dwordx4 v[54:57], v[4:5], off offset:256
	v_add_co_u32_e32 v2, vcc, s73, v64
	s_nop 1
	v_addc_co_u32_e32 v3, vcc, 0, v65, vcc
	v_add_co_u32_e32 v4, vcc, s73, v62
	global_load_dwordx4 v[42:45], v[2:3], off
	global_load_dwordx4 v[34:37], v[2:3], off offset:256
	v_addc_co_u32_e32 v5, vcc, 0, v63, vcc
	v_add_co_u32_e32 v2, vcc, s38, v64
	global_load_dwordx4 v[46:49], v[4:5], off
	global_load_dwordx4 v[38:41], v[4:5], off offset:256
	v_addc_co_u32_e32 v3, vcc, 0, v65, vcc
	v_add_co_u32_e32 v4, vcc, s38, v62
	global_load_dwordx4 v[26:29], v[2:3], off
	global_load_dwordx4 v[18:21], v[2:3], off offset:256
	v_addc_co_u32_e32 v5, vcc, 0, v63, vcc
	v_add_co_u32_e32 v2, vcc, s88, v64
	global_load_dwordx4 v[30:33], v[4:5], off
	global_load_dwordx4 v[22:25], v[4:5], off offset:256
	v_addc_co_u32_e32 v3, vcc, 0, v65, vcc
	v_add_co_u32_e32 v4, vcc, s88, v62
	s_nop 1
	v_addc_co_u32_e32 v5, vcc, 0, v63, vcc
	global_load_dwordx4 v[10:13], v[2:3], off
	global_load_dwordx4 v[6:9], v[2:3], off offset:256
	global_load_dwordx4 v[14:17], v[4:5], off
	s_nop 0
	global_load_dwordx4 v[2:5], v[4:5], off offset:256
	s_waitcnt vmcnt(18)
	v_mul_f32_e32 v221, 0x39800000, v216
	s_nop 0
	v_mul_f32_e32 v190, v190, v221
	v_mul_f32_e32 v186, v186, v221
	v_mul_f32_e32 v191, v191, v221
	v_mul_f32_e32 v216, v187, v221
	v_lshlrev_b32_e32 v62, 16, v224
	v_and_b32_e32 v63, 0xffff0000, v224
	v_mul_f32_e32 v190, 0xbfb8aa3b, v190
	v_mul_f32_e32 v223, 0xbfb8aa3b, v186
	v_mul_f32_e32 v191, 0xbfb8aa3b, v191
	v_mul_f32_e32 v224, 0xbfb8aa3b, v216
	v_exp_f32_e32 v190, v190
	v_exp_f32_e32 v223, v223
	v_exp_f32_e32 v191, v191
	v_exp_f32_e32 v224, v224
	v_add_f32_e32 v190, 1.0, v190
	v_add_f32_e32 v223, 1.0, v223
	v_add_f32_e32 v191, 1.0, v191
	v_add_f32_e32 v224, 1.0, v224
	v_rcp_f32_e32 v190, v190
	v_rcp_f32_e32 v232, v223
	v_rcp_f32_e32 v191, v191
	v_rcp_f32_e32 v233, v224
	v_mul_f32_e32 v192, v192, v221
	v_mul_f32_e32 v192, 0xbfb8aa3b, v192
	v_lshlrev_b32_e32 v64, 16, v226
	v_and_b32_e32 v65, 0xffff0000, v226
	v_exp_f32_e32 v192, v192
	v_mul_f32_e32 v189, v189, v221
	v_mul_f32_e32 v189, 0xbfb8aa3b, v189
	v_exp_f32_e32 v189, v189
	v_mul_f32_e32 v158, v158, v221
	v_mul_f32_e32 v159, v159, v221
	v_mul_f32_e32 v158, 0xbfb8aa3b, v158
	v_mul_f32_e32 v154, v154, v221
	v_mul_f32_e32 v159, 0xbfb8aa3b, v159
	v_exp_f32_e32 v158, v158
	v_mul_f32_e32 v154, 0xbfb8aa3b, v154
	v_exp_f32_e32 v159, v159
	v_exp_f32_e32 v154, v154
	v_add_f32_e32 v158, 1.0, v158
	v_rcp_f32_e32 v158, v158
	v_add_f32_e32 v159, 1.0, v159
	v_add_f32_e32 v154, 1.0, v154
	v_rcp_f32_e32 v159, v159
	v_rcp_f32_e32 v154, v154
	s_waitcnt vmcnt(17)
	v_lshlrev_b32_e32 v186, 16, v228
	v_and_b32_e32 v187, 0xffff0000, v228
	v_lshlrev_b32_e32 v216, 16, v230
	v_and_b32_e32 v217, 0xffff0000, v230
	v_pk_fma_f32 v[190:191], v[190:191], v[186:187], v[62:63]
	v_pk_fma_f32 v[186:187], v[232:233], v[216:217], v[64:65]
	v_mul_f32_e32 v65, v188, v221
	v_mul_f32_e32 v65, 0xbfb8aa3b, v65
	v_mul_f32_e32 v188, v193, v221
	v_exp_f32_e32 v65, v65
	v_mul_f32_e32 v188, 0xbfb8aa3b, v188
	v_add_f32_e32 v64, 1.0, v192
	v_exp_f32_e32 v192, v188
	v_add_f32_e32 v65, 1.0, v65
	v_rcp_f32_e32 v188, v65
	v_rcp_f32_e32 v64, v64
	v_add_f32_e32 v65, 1.0, v192
	v_rcp_f32_e32 v65, v65
	v_lshlrev_b32_e32 v192, 16, v225
	v_and_b32_e32 v193, 0xffff0000, v225
	v_lshlrev_b32_e32 v216, 16, v229
	v_and_b32_e32 v217, 0xffff0000, v229
	v_pk_fma_f32 v[192:193], v[64:65], v[216:217], v[192:193]
	v_add_f32_e32 v64, 1.0, v189
	v_rcp_f32_e32 v189, v64
	v_lshlrev_b32_e32 v64, 16, v227
	v_and_b32_e32 v65, 0xffff0000, v227
	v_lshlrev_b32_e32 v216, 16, v231
	v_and_b32_e32 v217, 0xffff0000, v231
	v_pk_fma_f32 v[188:189], v[188:189], v[216:217], v[64:65]
	s_waitcnt vmcnt(13)
	v_lshlrev_b32_e32 v216, 16, v50
	v_and_b32_e32 v217, 0xffff0000, v50
	v_mul_f32_e32 v50, v155, v221
	v_mul_f32_e32 v50, 0xbfb8aa3b, v50
	v_exp_f32_e32 v50, v50
	s_waitcnt vmcnt(12)
	v_lshlrev_b32_e32 v224, 16, v54
	v_and_b32_e32 v225, 0xffff0000, v54
	v_pk_fma_f32 v[158:159], v[158:159], v[224:225], v[216:217]
	v_add_f32_e32 v50, 1.0, v50
	v_rcp_f32_e32 v155, v50
	v_mul_f32_e32 v50, v160, v221
	v_lshlrev_b32_e32 v216, 16, v52
	v_and_b32_e32 v217, 0xffff0000, v52
	v_lshlrev_b32_e32 v224, 16, v56
	v_and_b32_e32 v225, 0xffff0000, v56
	v_mul_f32_e32 v50, 0xbfb8aa3b, v50
	v_mul_f32_e32 v52, v156, v221
	v_mul_f32_e32 v54, v161, v221
	v_exp_f32_e32 v50, v50
	v_pk_fma_f32 v[154:155], v[154:155], v[224:225], v[216:217]
	v_mul_f32_e32 v52, 0xbfb8aa3b, v52
	v_mul_f32_e32 v54, 0xbfb8aa3b, v54
	v_lshlrev_b32_e32 v224, 16, v51
	v_and_b32_e32 v225, 0xffff0000, v51
	v_mul_f32_e32 v51, v157, v221
	v_exp_f32_e32 v52, v52
	v_exp_f32_e32 v54, v54
	v_mul_f32_e32 v51, 0xbfb8aa3b, v51
	v_exp_f32_e32 v51, v51
	v_add_f32_e32 v50, 1.0, v50
	v_rcp_f32_e32 v160, v50
	v_add_f32_e32 v50, 1.0, v52
	v_add_f32_e32 v52, 1.0, v54
	v_rcp_f32_e32 v161, v52
	v_add_f32_e32 v51, 1.0, v51
	v_rcp_f32_e32 v50, v50
	v_rcp_f32_e32 v51, v51
	v_pk_mul_f32 v[62:63], v[186:187], v[186:187]
	v_lshlrev_b32_e32 v54, 16, v55
	v_and_b32_e32 v55, 0xffff0000, v55
	v_pk_fma_f32 v[62:63], v[190:191], v[190:191], v[62:63]
	v_pk_mul_f32 v[64:65], v[188:189], v[188:189]
	v_pk_fma_f32 v[160:161], v[160:161], v[54:55], v[224:225]
	v_lshlrev_b32_e32 v52, 16, v53
	v_and_b32_e32 v53, 0xffff0000, v53
	v_lshlrev_b32_e32 v54, 16, v57
	v_and_b32_e32 v55, 0xffff0000, v57
	v_pk_fma_f32 v[64:65], v[192:193], v[192:193], v[64:65]
	v_pk_fma_f32 v[156:157], v[50:51], v[54:55], v[52:53]
	v_add_f32_e32 v52, v62, v63
	v_pk_mul_f32 v[216:217], v[154:155], v[154:155]
	v_add_f32_e32 v52, v64, v52
	v_pk_fma_f32 v[216:217], v[158:159], v[158:159], v[216:217]
	v_add_f32_e32 v52, v65, v52
	v_pk_mul_f32 v[50:51], v[156:157], v[156:157]
	v_add_f32_e32 v52, v216, v52
	v_pk_fma_f32 v[50:51], v[160:161], v[160:161], v[50:51]
	v_add_f32_e32 v52, v217, v52
	v_add_f32_e32 v50, v50, v52
	v_add_f32_e32 v50, v51, v50
	ds_bpermute_b32 v51, v201, v50
	s_waitcnt lgkmcnt(0)
	v_add_f32_e32 v50, v50, v51
	ds_bpermute_b32 v51, v205, v50
	s_and_saveexec_b64 s[6:7], s[0:1]
	s_cbranch_execz .LBB0_1364
	s_waitcnt lgkmcnt(0)
	v_add_f32_e32 v50, v50, v51
	global_atomic_add_f32 v[60:61], v50, off offset:512

.LBB0_1376:
	s_or_b64 exec, exec, s[6:7]
	v_or_b32_e32 v2, s2, v194
	s_waitcnt lgkmcnt(0)
	v_ashrrev_i32_e32 v3, 31, v2
	s_barrier
	v_lshl_add_u64 v[6:7], v[2:3], 2, s[78:79]
	global_load_dwordx4 v[10:13], v[6:7], off offset:16
	global_load_dwordx4 v[14:17], v[6:7], off
	global_load_dwordx4 v[2:5], v[6:7], off offset:528
	s_nop 0
	global_load_dwordx4 v[6:9], v[6:7], off offset:512
	s_nop 0
	global_load_dword v19, v[60:61], off sc1
	global_load_dword v18, v[60:61], off offset:64 sc1
	global_load_dword v244, v[60:61], off offset:128 sc1
	global_load_dword v243, v[60:61], off offset:192 sc1
	global_load_dword v246, v[60:61], off offset:512 sc1
	global_load_dword v245, v[60:61], off offset:576 sc1
	global_load_dword v248, v[60:61], off offset:640 sc1
	global_load_dword v247, v[60:61], off offset:704 sc1
	s_mov_b32 s2, 0x358637bd
	v_mov_b64_e32 v[24:25], s[2:3]
	s_mov_b64 s[2:3], 0x20000
	s_waitcnt vmcnt(0)
	v_pk_fma_f32 v[18:19], v[18:19], s[36:37], v[24:25] op_sel_hi:[1,0,0]
	s_nop 0
	v_mul_f32_e32 v20, 0x4b800000, v19
	v_cmp_gt_f32_e64 s[6:7], s89, v19
	v_cmp_gt_f32_e32 vcc, s89, v18
	s_nop 0
	v_cndmask_b32_e64 v19, v19, v20, s[6:7]
	v_rsq_f32_e32 v19, v19
	s_nop 0
	v_mul_f32_e32 v20, 0x45800000, v19
	v_cndmask_b32_e64 v34, v19, v20, s[6:7]
	v_mul_f32_e32 v19, 0x4b800000, v18
	v_cndmask_b32_e32 v18, v18, v19, vcc
	v_rsq_f32_e32 v18, v18
	v_pk_mul_f32 v[32:33], v[66:67], v[34:35] op_sel_hi:[1,0]
	v_pk_mul_f32 v[36:37], v[68:69], v[34:35] op_sel_hi:[1,0]
	v_pk_mul_f32 v[40:41], v[128:129], v[34:35] op_sel_hi:[1,0]
	v_mul_f32_e32 v19, 0x45800000, v18
	v_cndmask_b32_e32 v26, v18, v19, vcc
	v_mov_b32_e32 v19, v244
	v_mov_b32_e32 v18, v243
	v_pk_mul_f32 v[38:39], v[16:17], v[36:37]
	v_pk_mul_f32 v[36:37], v[14:15], v[32:33]
	v_pk_mul_f32 v[32:33], v[126:127], v[34:35] op_sel_hi:[1,0]
	v_pk_mul_f32 v[42:43], v[12:13], v[40:41]
	v_pk_mul_f32 v[40:41], v[10:11], v[32:33]
	v_lshl_add_u64 v[32:33], v[58:59], 2, s[80:81]
	s_waitcnt vmcnt(0)
	v_pk_fma_f32 v[18:19], v[18:19], s[36:37], v[24:25] op_sel_hi:[1,0,0]
	s_nop 0
	v_mul_f32_e32 v20, 0x4b800000, v19
	v_cmp_gt_f32_e64 s[6:7], s89, v19
	v_cmp_gt_f32_e32 vcc, s89, v18
	s_nop 0
	v_cndmask_b32_e64 v19, v19, v20, s[6:7]
	v_rsq_f32_e32 v19, v19
	s_nop 0
	v_mul_f32_e32 v20, 0x45800000, v19
	v_cndmask_b32_e64 v30, v19, v20, s[6:7]
	v_mul_f32_e32 v19, 0x4b800000, v18
	v_cndmask_b32_e32 v18, v18, v19, vcc
	v_rsq_f32_e32 v18, v18
	s_nop 0
	v_mul_f32_e32 v19, 0x45800000, v18
	v_cndmask_b32_e32 v22, v18, v19, vcc
	v_mov_b32_e32 v19, v246
	v_mov_b32_e32 v18, v245
	s_waitcnt vmcnt(0)
	v_pk_fma_f32 v[18:19], v[18:19], s[36:37], v[24:25] op_sel_hi:[1,0,0]
	s_nop 0
	v_mul_f32_e32 v20, 0x4b800000, v19
	v_cmp_gt_f32_e64 s[6:7], s89, v19
	v_cmp_gt_f32_e32 vcc, s89, v18
	s_nop 0
	v_cndmask_b32_e64 v19, v19, v20, s[6:7]
	v_rsq_f32_e32 v19, v19
	s_nop 0
	v_mul_f32_e32 v20, 0x45800000, v19
	v_cndmask_b32_e64 v28, v19, v20, s[6:7]
	v_mul_f32_e32 v19, 0x4b800000, v18
	v_cndmask_b32_e32 v18, v18, v19, vcc
	v_rsq_f32_e32 v18, v18
	s_nop 0
	v_mul_f32_e32 v19, 0x45800000, v18
	v_cndmask_b32_e32 v20, v18, v19, vcc
	v_mov_b32_e32 v19, v248
	v_mov_b32_e32 v18, v247
	s_nop 0
	global_store_dwordx4 v[32:33], v[36:39], off
	global_store_dwordx4 v[32:33], v[40:43], off offset:16
	s_waitcnt vmcnt(2)
	v_pk_fma_f32 v[18:19], v[18:19], s[36:37], v[24:25] op_sel_hi:[1,0,0]
	s_nop 0
	v_mul_f32_e32 v21, 0x4b800000, v19
	v_cmp_gt_f32_e64 s[6:7], s89, v19
	v_cmp_gt_f32_e32 vcc, s89, v18
	v_pk_mul_f32 v[36:37], v[98:99], v[34:35] op_sel_hi:[1,0]
	v_cndmask_b32_e64 v19, v19, v21, s[6:7]
	v_rsq_f32_e32 v19, v19
	v_pk_mul_f32 v[38:39], v[100:101], v[34:35] op_sel_hi:[1,0]
	v_pk_mul_f32 v[36:37], v[6:7], v[36:37]
	v_pk_mul_f32 v[38:39], v[8:9], v[38:39]
	v_mul_f32_e32 v21, 0x45800000, v19
	v_cndmask_b32_e64 v24, v19, v21, s[6:7]
	v_mul_f32_e32 v19, 0x4b800000, v18
	v_cndmask_b32_e32 v18, v18, v19, vcc
	v_rsq_f32_e32 v18, v18
	v_pk_mul_f32 v[40:41], v[94:95], v[34:35] op_sel_hi:[1,0]
	v_pk_mul_f32 v[34:35], v[96:97], v[34:35] op_sel_hi:[1,0]
	v_pk_mul_f32 v[40:41], v[2:3], v[40:41]
	v_mul_f32_e32 v19, 0x45800000, v18
	v_cndmask_b32_e32 v18, v18, v19, vcc
	v_pk_mul_f32 v[42:43], v[4:5], v[34:35]
	global_store_dwordx4 v[32:33], v[36:39], off offset:512
	global_store_dwordx4 v[32:33], v[40:43], off offset:528
	v_pk_mul_f32 v[34:35], v[122:123], v[26:27] op_sel_hi:[1,0]
	v_pk_mul_f32 v[36:37], v[124:125], v[26:27] op_sel_hi:[1,0]
	v_add_co_u32_e32 v44, vcc, s77, v32
	v_pk_mul_f32 v[36:37], v[16:17], v[36:37]
	v_pk_mul_f32 v[34:35], v[14:15], v[34:35]
	v_pk_mul_f32 v[38:39], v[118:119], v[26:27] op_sel_hi:[1,0]
	v_pk_mul_f32 v[40:41], v[120:121], v[26:27] op_sel_hi:[1,0]
	v_addc_co_u32_e32 v45, vcc, 0, v33, vcc
	v_pk_mul_f32 v[40:41], v[12:13], v[40:41]
	v_pk_mul_f32 v[38:39], v[10:11], v[38:39]
	v_lshl_add_u64 v[42:43], v[32:33], 0, s[2:3]
	global_store_dwordx4 v[44:45], v[34:37], off
	global_store_dwordx4 v[42:43], v[38:41], off offset:16
	s_mov_b64 s[2:3], 0x40000
	v_pk_mul_f32 v[34:35], v[90:91], v[26:27] op_sel_hi:[1,0]
	v_pk_mul_f32 v[36:37], v[92:93], v[26:27] op_sel_hi:[1,0]
	v_pk_mul_f32 v[34:35], v[6:7], v[34:35]
	v_pk_mul_f32 v[36:37], v[8:9], v[36:37]
	v_pk_mul_f32 v[38:39], v[86:87], v[26:27] op_sel_hi:[1,0]
	v_pk_mul_f32 v[26:27], v[88:89], v[26:27] op_sel_hi:[1,0]
	v_pk_mul_f32 v[38:39], v[2:3], v[38:39]
	v_pk_mul_f32 v[40:41], v[4:5], v[26:27]
	global_store_dwordx4 v[42:43], v[34:37], off offset:512
	global_store_dwordx4 v[42:43], v[38:41], off offset:528
	v_pk_mul_f32 v[26:27], v[114:115], v[30:31] op_sel_hi:[1,0]
	v_pk_mul_f32 v[34:35], v[116:117], v[30:31] op_sel_hi:[1,0]
	v_pk_mul_f32 v[38:39], v[112:113], v[30:31] op_sel_hi:[1,0]
	v_pk_mul_f32 v[36:37], v[16:17], v[34:35]
	v_pk_mul_f32 v[34:35], v[14:15], v[26:27]
	v_pk_mul_f32 v[26:27], v[110:111], v[30:31] op_sel_hi:[1,0]
	v_add_co_u32_e32 v42, vcc, s90, v32
	v_pk_mul_f32 v[40:41], v[12:13], v[38:39]
	v_pk_mul_f32 v[38:39], v[10:11], v[26:27]
	v_addc_co_u32_e32 v43, vcc, 0, v33, vcc
	v_lshl_add_u64 v[26:27], v[32:33], 0, s[2:3]
	global_store_dwordx4 v[42:43], v[34:37], off
	global_store_dwordx4 v[26:27], v[38:41], off offset:16
	s_nop 0
	v_pk_mul_f32 v[34:35], v[82:83], v[30:31] op_sel_hi:[1,0]
	v_pk_mul_f32 v[36:37], v[84:85], v[30:31] op_sel_hi:[1,0]
	v_pk_mul_f32 v[38:39], v[78:79], v[30:31] op_sel_hi:[1,0]
	v_pk_mul_f32 v[30:31], v[80:81], v[30:31] op_sel_hi:[1,0]
	v_pk_mul_f32 v[36:37], v[8:9], v[36:37]
	v_pk_mul_f32 v[34:35], v[6:7], v[34:35]
	v_pk_mul_f32 v[40:41], v[4:5], v[30:31]
	v_pk_mul_f32 v[30:31], v[108:109], v[22:23] op_sel_hi:[1,0]
	v_pk_mul_f32 v[38:39], v[2:3], v[38:39]
	global_store_dwordx4 v[26:27], v[34:37], off offset:512
	global_store_dwordx4 v[26:27], v[38:41], off offset:528
	v_pk_mul_f32 v[26:27], v[106:107], v[22:23] op_sel_hi:[1,0]
	v_pk_mul_f32 v[36:37], v[16:17], v[30:31]
	v_pk_mul_f32 v[30:31], v[104:105], v[22:23] op_sel_hi:[1,0]
	v_pk_mul_f32 v[34:35], v[14:15], v[26:27]
	v_pk_mul_f32 v[40:41], v[12:13], v[30:31]
	v_add_co_u32_e32 v30, vcc, s91, v32
	v_pk_mul_f32 v[26:27], v[102:103], v[22:23] op_sel_hi:[1,0]
	s_nop 0
	v_addc_co_u32_e32 v31, vcc, 0, v33, vcc
	v_pk_mul_f32 v[38:39], v[10:11], v[26:27]
	v_lshl_add_u64 v[26:27], v[32:33], 0, s[40:41]
	global_store_dwordx4 v[30:31], v[34:37], off
	global_store_dwordx4 v[26:27], v[38:41], off offset:16
	v_pk_mul_f32 v[30:31], v[74:75], v[22:23] op_sel_hi:[1,0]
	v_pk_mul_f32 v[34:35], v[76:77], v[22:23] op_sel_hi:[1,0]
	s_nop 0
	v_pk_mul_f32 v[36:37], v[8:9], v[34:35]
	v_pk_mul_f32 v[34:35], v[6:7], v[30:31]
	v_pk_mul_f32 v[30:31], v[70:71], v[22:23] op_sel_hi:[1,0]
	v_pk_mul_f32 v[22:23], v[72:73], v[22:23] op_sel_hi:[1,0]
	v_pk_mul_f32 v[38:39], v[2:3], v[30:31]
	v_pk_mul_f32 v[40:41], v[4:5], v[22:23]
	global_store_dwordx4 v[26:27], v[34:37], off offset:512
	global_store_dwordx4 v[26:27], v[38:41], off offset:528
	v_pk_mul_f32 v[26:27], v[192:193], v[28:29] op_sel_hi:[1,0]
	v_pk_mul_f32 v[22:23], v[190:191], v[28:29] op_sel_hi:[1,0]
	v_pk_mul_f32 v[36:37], v[16:17], v[26:27]
	v_pk_mul_f32 v[26:27], v[188:189], v[28:29] op_sel_hi:[1,0]
	v_pk_mul_f32 v[34:35], v[14:15], v[22:23]
	v_pk_mul_f32 v[40:41], v[12:13], v[26:27]
	v_add_co_u32_e32 v26, vcc, s92, v32
	v_pk_mul_f32 v[22:23], v[186:187], v[28:29] op_sel_hi:[1,0]
	s_nop 0
	v_addc_co_u32_e32 v27, vcc, 0, v33, vcc
	v_pk_mul_f32 v[38:39], v[10:11], v[22:23]
	v_lshl_add_u64 v[22:23], v[32:33], 0, s[42:43]
	global_store_dwordx4 v[26:27], v[34:37], off
	global_store_dwordx4 v[22:23], v[38:41], off offset:16
	v_pk_mul_f32 v[26:27], v[158:159], v[28:29] op_sel_hi:[1,0]
	v_pk_mul_f32 v[30:31], v[160:161], v[28:29] op_sel_hi:[1,0]
	v_pk_mul_f32 v[34:35], v[6:7], v[26:27]
	v_pk_mul_f32 v[26:27], v[154:155], v[28:29] op_sel_hi:[1,0]
	v_pk_mul_f32 v[36:37], v[8:9], v[30:31]
	v_pk_mul_f32 v[28:29], v[156:157], v[28:29] op_sel_hi:[1,0]
	v_pk_mul_f32 v[26:27], v[2:3], v[26:27]
	v_pk_mul_f32 v[28:29], v[4:5], v[28:29]
	global_store_dwordx4 v[22:23], v[34:37], off offset:512
	global_store_dwordx4 v[22:23], v[26:29], off offset:528
	v_pk_mul_f32 v[22:23], v[182:183], v[20:21] op_sel_hi:[1,0]
	v_pk_mul_f32 v[30:31], v[180:181], v[20:21] op_sel_hi:[1,0]
	v_pk_mul_f32 v[26:27], v[184:185], v[20:21] op_sel_hi:[1,0]
	v_pk_mul_f32 v[36:37], v[12:13], v[30:31]
	v_pk_mul_f32 v[28:29], v[16:17], v[26:27]
	v_pk_mul_f32 v[26:27], v[14:15], v[22:23]
	v_pk_mul_f32 v[22:23], v[178:179], v[20:21] op_sel_hi:[1,0]
	v_lshl_add_u64 v[30:31], v[32:33], 0, s[44:45]
	v_pk_mul_f32 v[34:35], v[10:11], v[22:23]
	v_add_co_u32_e32 v22, vcc, s93, v32
	s_nop 1
	v_addc_co_u32_e32 v23, vcc, 0, v33, vcc
	global_store_dwordx4 v[22:23], v[26:29], off
	global_store_dwordx4 v[30:31], v[34:37], off offset:16
	v_pk_mul_f32 v[22:23], v[150:151], v[20:21] op_sel_hi:[1,0]
	v_pk_mul_f32 v[26:27], v[152:153], v[20:21] op_sel_hi:[1,0]
	v_pk_mul_f32 v[34:35], v[146:147], v[20:21] op_sel_hi:[1,0]
	v_pk_mul_f32 v[20:21], v[148:149], v[20:21] op_sel_hi:[1,0]
	v_pk_mul_f32 v[28:29], v[8:9], v[26:27]
	v_pk_mul_f32 v[26:27], v[6:7], v[22:23]
	v_pk_mul_f32 v[22:23], v[4:5], v[20:21]
	v_pk_mul_f32 v[20:21], v[2:3], v[34:35]
	global_store_dwordx4 v[30:31], v[26:29], off offset:512
	global_store_dwordx4 v[30:31], v[20:23], off offset:528
	v_add_co_u32_e32 v34, vcc, s94, v32
	s_nop 0
	v_pk_mul_f32 v[20:21], v[174:175], v[24:25] op_sel_hi:[1,0]
	v_pk_mul_f32 v[22:23], v[176:177], v[24:25] op_sel_hi:[1,0]
	v_pk_mul_f32 v[20:21], v[14:15], v[20:21]
	v_pk_mul_f32 v[22:23], v[16:17], v[22:23]
	v_pk_mul_f32 v[26:27], v[170:171], v[24:25] op_sel_hi:[1,0]
	v_pk_mul_f32 v[28:29], v[172:173], v[24:25] op_sel_hi:[1,0]
	v_addc_co_u32_e32 v35, vcc, 0, v33, vcc
	v_pk_mul_f32 v[28:29], v[12:13], v[28:29]
	v_pk_mul_f32 v[26:27], v[10:11], v[26:27]
	v_lshl_add_u64 v[30:31], v[32:33], 0, s[46:47]
	global_store_dwordx4 v[34:35], v[20:23], off
	global_store_dwordx4 v[30:31], v[26:29], off offset:16
	s_nop 0
	v_pk_mul_f32 v[20:21], v[142:143], v[24:25] op_sel_hi:[1,0]
	v_pk_mul_f32 v[22:23], v[144:145], v[24:25] op_sel_hi:[1,0]
	v_pk_mul_f32 v[20:21], v[6:7], v[20:21]
	v_pk_mul_f32 v[22:23], v[8:9], v[22:23]
	v_pk_mul_f32 v[28:29], v[138:139], v[24:25] op_sel_hi:[1,0]
	v_pk_mul_f32 v[24:25], v[140:141], v[24:25] op_sel_hi:[1,0]
	s_nop 0
	v_pk_mul_f32 v[26:27], v[4:5], v[24:25]
	v_pk_mul_f32 v[24:25], v[2:3], v[28:29]
	global_store_dwordx4 v[30:31], v[20:23], off offset:512
	global_store_dwordx4 v[30:31], v[24:27], off offset:528
	s_nop 0
	v_pk_mul_f32 v[22:23], v[168:169], v[18:19] op_sel_hi:[1,0]
	v_pk_mul_f32 v[20:21], v[166:167], v[18:19] op_sel_hi:[1,0]
	v_pk_mul_f32 v[16:17], v[16:17], v[22:23]
	v_pk_mul_f32 v[22:23], v[164:165], v[18:19] op_sel_hi:[1,0]
	v_pk_mul_f32 v[14:15], v[14:15], v[20:21]
	v_pk_mul_f32 v[20:21], v[162:163], v[18:19] op_sel_hi:[1,0]
	v_pk_mul_f32 v[12:13], v[12:13], v[22:23]
	v_add_co_u32_e32 v22, vcc, s95, v32
	v_pk_mul_f32 v[10:11], v[10:11], v[20:21]
	s_nop 0
	v_addc_co_u32_e32 v23, vcc, 0, v33, vcc
	v_lshl_add_u64 v[20:21], v[32:33], 0, s[48:49]
	global_store_dwordx4 v[22:23], v[14:17], off
	global_store_dwordx4 v[20:21], v[10:13], off offset:16
	s_andn2_b64 vcc, exec, s[22:23]
	s_nop 0
	v_pk_mul_f32 v[10:11], v[134:135], v[18:19] op_sel_hi:[1,0]
	v_pk_mul_f32 v[12:13], v[136:137], v[18:19] op_sel_hi:[1,0]
	v_pk_mul_f32 v[6:7], v[6:7], v[10:11]
	v_pk_mul_f32 v[8:9], v[8:9], v[12:13]
	v_pk_mul_f32 v[10:11], v[130:131], v[18:19] op_sel_hi:[1,0]
	v_pk_mul_f32 v[12:13], v[132:133], v[18:19] op_sel_hi:[1,0]
	v_pk_mul_f32 v[2:3], v[2:3], v[10:11]
	v_pk_mul_f32 v[4:5], v[4:5], v[12:13]
	global_store_dwordx4 v[20:21], v[6:9], off offset:512
	global_store_dwordx4 v[20:21], v[2:5], off offset:528
	s_cbranch_vccnz .LBB0_1388
	s_mov_b64 s[22:23], 0
	s_cmp_gt_i32 s28, 0x3ffffffd
	s_mov_b32 s3, s20
	s_mov_b32 s6, s62
	s_cbranch_scc1 .LBB0_1384
	s_ashr_i32 s29, s28, 31
	s_lshl_b64 s[2:3], s[28:29], 8
	s_add_u32 s2, s2, s87
	s_addc_u32 s3, s3, s39
	s_add_u32 s2, s2, 0x200
	s_addc_u32 s3, s3, 0
	v_cmp_gt_i64_e32 vcc, s[2:3], v[212:213]
	s_mov_b32 s6, s62
	s_mov_b32 s3, s20
	s_cbranch_vccnz .LBB0_1384
	s_ashr_i32 s3, s2, 31
	s_lshr_b32 s3, s3, 29
	s_add_i32 s6, s2, s3
	s_and_b32 s3, s6, -8
	s_sub_i32 s7, s2, s3
	s_cmp_gt_i32 s7, -1
	s_mov_b64 s[2:3], -1
	s_cbranch_scc0 .LBB0_1381
	s_lshl_b32 s18, s7, 6
	s_mov_b64 s[2:3], 0
